# HGRN chunk phases: lower-bound load prefetched one unit ahead so the unit-opening vmcnt(0) no longer drains the next unit's LDS-DMA prefetch
# speedup vs baseline: 1.0021x; 1.0021x over previous
; #define LAS __attribute__((address_space(3)))
; #define HGL_COLS() do { asm volatile("s_waitcnt vmcnt(0)" ::: "memory"); _Pragma("unroll") for (int i = 0; i < 16; ++i) { fl[i] = *(const LAS unsigned short*)(ZW + i * 128 + c.lane * 2); vv[i] = *(const LAS unsigned short*)(ZW + 2048 + i * 128 + c.lane * 2); } \
;         asm volatile("s_waitcnt lgkmcnt(0)" ::: "memory"); } while (0)
; __device__ __forceinline__ void ph_hgL(const Ctx& c) {
;     const bf16* ZH = WSP(bf16, WS_XB); const float* lb = WSP(float, WS_LB); float* KV = WSP(float, WS_KV); float* DEC = WSP(float, WS_HGDEC);
;     LAS bf16* VT = (LAS bf16*)c.lds; LAS bf16* KT = VT + 128 * 72; LAS float* SS = (LAS float*)(KT + 128 * 72); LAS bf16* ST = (LAS bf16*)(c.lds + 65536);
;     const int d = c.tid & 127, seg = c.tid >> 7, r = c.lane & 31, hh = c.lane >> 5, w = c.wave;
;     unsigned short fl[16], vv[16];
;     LAS unsigned char* ZW = c.lds + 107520 + w * 4096;
;     const int zr = c.lane >> 3, zp = c.lane & 7;
;     ...
;     if (c.bid < 2048) { HGL_DMA(c.bid); HGL_COLS(); }
.LBB0_453:
	s_or_b64 exec, exec, s[0:1]
	s_cmpk_gt_i32 s2, 0x7ff
	s_cbranch_scc1 .LBB0_462
	s_add_u32 s12, s46, 0x66b00000
	v_readlane_b32 s24, v254, 46
	s_addc_u32 s13, s47, 0
	s_lshl_b32 s0, s24, 12
	s_add_i32 s3, s0, 0
	s_add_i32 s33, s3, 0x1a400
	s_add_u32 s4, s46, 0x43500000
	v_ashrrev_i32_e32 v0, 3, v50
	v_ashrrev_i32_e32 v8, 7, v24
	s_addc_u32 s5, s47, 0
	s_ashr_i32 s0, s2, 7
	s_ashr_i32 s1, s0, 31
	s_lshl_b32 s6, s2, 6
	v_lshl_add_u32 v40, v8, 4, v0
	s_mov_b32 s15, 0
	s_and_b32 s14, s6, 0x1fc0
	v_ashrrev_i32_e32 v41, 31, v40
	s_lshl_b64 s[0:1], s[0:1], 21
	v_lshl_add_u64 v[0:1], s[14:15], 0, v[40:41]
	s_add_u32 s0, s4, s0
	v_lshlrev_b64 v[0:1], 8, v[0:1]
	s_addc_u32 s1, s5, s1
	v_lshl_add_u64 v[0:1], s[0:1], 0, v[0:1]
	v_readlane_b32 s0, v254, 4
	s_and_b32 s0, s0, 64
	v_and_b32_e32 v2, 7, v50
	s_lshl_b32 s14, s0, 1
	v_lshl_add_u64 v[0:1], v[0:1], 0, s[14:15]
	v_lshlrev_b32_e32 v2, 4, v2
	v_mov_b32_e32 v3, 0
	v_lshl_add_u64 v[0:1], v[0:1], 0, v[2:3]
	s_mov_b64 s[16:17], 0x2000000
	v_lshl_add_u64 v[4:5], v[0:1], 0, s[16:17]
	s_mov_b32 m0, s33
	s_mov_b64 s[18:19], 0x2000800
	global_load_lds_dwordx4 v[4:5], off
	v_lshl_add_u64 v[4:5], v[0:1], 0, s[18:19]
	s_add_i32 m0, s3, 0x1a800
	s_mov_b64 s[20:21], 0x4000000
	global_load_lds_dwordx4 v[4:5], off
	v_lshl_add_u64 v[4:5], v[0:1], 0, s[20:21]
	s_add_i32 m0, s3, 0x1ac00
	s_mov_b64 s[22:23], 0x4000800
	global_load_lds_dwordx4 v[4:5], off
	v_lshl_add_u64 v[0:1], v[0:1], 0, s[22:23]
	s_add_i32 m0, s3, 0x1b000
	s_add_u32 s0, s4, s14
	global_load_lds_dwordx4 v[0:1], off
	v_lshlrev_b32_e32 v0, 1, v50
	s_waitcnt vmcnt(0)
	v_add_u32_e32 v55, s33, v0
	v_and_b32_e32 v54, 0x7f, v24
	ds_read_u16 v56, v55
	ds_read_u16 v57, v55 offset:128
	ds_read_u16 v58, v55 offset:256
	ds_read_u16 v59, v55 offset:384
	ds_read_u16 v60, v55 offset:512
	ds_read_u16 v61, v55 offset:640
	ds_read_u16 v62, v55 offset:768
	ds_read_u16 v63, v55 offset:896
	ds_read_u16 v0, v55 offset:2048
	ds_read_u16 v1, v55 offset:2176
	ds_read_u16 v4, v55 offset:2304
	ds_read_u16 v5, v55 offset:2432
	ds_read_u16 v9, v55 offset:2560
	ds_read_u16 v10, v55 offset:2688
	ds_read_u16 v11, v55 offset:2816
	ds_read_u16 v12, v55 offset:2944
	ds_read_u16 v13, v55 offset:3072
	ds_read_u16 v14, v55 offset:3200
	ds_read_u16 v15, v55 offset:3328
	ds_read_u16 v16, v55 offset:3456
	ds_read_u16 v17, v55 offset:3584
	ds_read_u16 v18, v55 offset:3712
	ds_read_u16 v19, v55 offset:3840
	ds_read_u16 v20, v55 offset:3968
	ds_read_u16 v67, v55 offset:1024
	ds_read_u16 v68, v55 offset:1152
	ds_read_u16 v69, v55 offset:1280
	ds_read_u16 v70, v55 offset:1408
	ds_read_u16 v71, v55 offset:1536
	ds_read_u16 v72, v55 offset:1664
	ds_read_u16 v74, v55 offset:1792
	ds_read_u16 v75, v55 offset:1920
	s_mov_b32 s36, 0x5040100
	s_addc_u32 s1, s5, 0
	s_lshl_b32 s14, s24, 4
	v_and_b32_e32 v6, 31, v50
	s_waitcnt lgkmcnt(0)
	v_perm_b32 v36, v1, v0, s36
	v_lshl_add_u32 v65, v54, 2, 0
	v_mul_u32_u24_e32 v0, 0x8c, v54
	v_lshlrev_b32_e32 v1, 5, v8
	s_movk_i32 s3, 0x80
	s_and_b32 s14, s14, 0x3fffffe0
	v_ashrrev_i32_e32 v7, 5, v50
	v_add3_u32 v66, v65, v0, v1
	v_cmp_gt_u32_e64 s[8:9], s3, v24
	s_lshl_b32 s3, s24, 1
	v_or_b32_e32 v0, s14, v6
	s_movk_i32 s24, 0x90
	s_and_b32 s3, s3, 2
	v_mul_lo_u32 v0, v0, s24
	v_lshlrev_b32_e32 v1, 4, v7
	v_add3_u32 v73, 0, v0, v1
	v_lshl_or_b32 v0, s3, 5, v6
	v_mul_u32_u24_e32 v0, 0x90, v0
	v_add3_u32 v76, 0, v0, v1
	v_lshl_add_u32 v0, v7, 2, s14
	s_lshl_b32 s3, s3, 6
	s_add_i32 s14, 0, 0x10000
	s_movk_i32 s24, 0x110
	s_add_i32 s3, s14, s3
	v_mul_lo_u32 v0, v0, s24
	v_lshlrev_b32_e32 v1, 1, v6
	v_add3_u32 v77, s3, v0, v1
	v_ashrrev_i32_e32 v0, 4, v24
	s_ashr_i32 s3, s2, 31
	v_mov_b32_e32 v25, v3
	v_mul_lo_u32 v1, v0, s24
	s_lshl_b64 s[24:25], s[2:3], 9
	v_perm_b32 v38, v10, v9, s36
	v_lshl_add_u64 v[42:43], s[0:1], 0, v[2:3]
	v_cmp_lt_i32_e64 s[0:1], 0, v8
	v_cmp_lt_i32_e64 s[4:5], 1, v8
	v_cmp_lt_i32_e64 s[6:7], 2, v8
	v_lshlrev_b32_e32 v2, 4, v50
	v_lshl_add_u64 v[8:9], v[24:25], 2, s[24:25]
	s_mov_b64 s[24:25], 0x66a00000
	v_and_b32_e32 v2, 0xf0, v2
	v_lshlrev_b32_e32 v0, 7, v0
	v_lshl_add_u64 v[44:45], v[8:9], 0, s[24:25]
	s_lshl_b64 s[26:27], s[2:3], 15
	v_and_b32_e32 v8, 15, v50
	v_add3_u32 v78, s14, v1, v2
	v_ashrrev_i32_e32 v1, 31, v0
	v_add_u32_e32 v2, 0x1000, v0
	v_lshl_or_b32 v8, v8, 4, s26
	v_mov_b32_e32 v9, s27
	v_perm_b32 v37, v5, v4, s36
	v_ashrrev_i32_e32 v3, 31, v2
	v_add_u32_e32 v4, 0x2000, v0
	v_add_u32_e32 v6, 0x3000, v0
	v_lshl_add_u64 v[0:1], v[0:1], 1, v[8:9]
	s_mov_b64 s[28:29], 0x59500000
	v_ashrrev_i32_e32 v5, 31, v4
	v_lshl_add_u64 v[46:47], v[0:1], 0, s[28:29]
	v_lshl_add_u64 v[0:1], v[2:3], 1, v[8:9]
	s_waitcnt lgkmcnt(0)
	v_ashrrev_i32_e32 v7, 31, v6
	v_lshl_add_u64 v[48:49], v[0:1], 0, s[28:29]
	v_lshl_add_u64 v[0:1], v[4:5], 1, v[8:9]
	s_ashr_i32 s97, s96, 31
	v_lshl_add_u64 v[50:51], v[0:1], 0, s[28:29]
	v_lshl_add_u64 v[0:1], v[6:7], 1, v[8:9]
	s_add_i32 s3, s2, s96
	v_perm_b32 v35, v20, v19, s36
	v_perm_b32 v34, v18, v17, s36
	v_perm_b32 v33, v16, v15, s36
	v_perm_b32 v32, v14, v13, s36
	v_perm_b32 v39, v12, v11, s36
	v_lshl_add_u32 v64, v24, 2, 0
	v_add_u32_e32 v79, 0x2200, v78
	v_add_u32_e32 v80, 0x4400, v78
	v_add_u32_e32 v81, 0x6600, v78
	s_lshl_b64 s[24:25], s[96:97], 9
	s_lshl_b64 s[26:27], s[96:97], 15
	v_lshl_add_u64 v[52:53], v[0:1], 0, s[28:29]
	s_lshl_b32 s3, s3, 6
	s_lshl_b32 s37, s96, 6
	s_add_i32 s38, s33, 0x400
	s_add_i32 s39, s33, 0x800
	s_add_i32 s40, s33, 0xc00
	s_mov_b32 s34, s2
	v_mov_b32_e32 v102, s34
	v_and_b32_e32 v102, 0x380, v102
	v_or_b32_e32 v102, v102, v54
	v_lshlrev_b32_e32 v102, 2, v102
	global_load_dword v102, v102, s[12:13]
	s_waitcnt vmcnt(0)
	s_branch .LBB0_456

; #define LAS __attribute__((address_space(3)))
; __device__ __forceinline__ float bf2f(bf16 b) { return __uint_as_float(((unsigned)b) << 16); }
; __device__ __forceinline__ float sigmoidf_(float x) { return __builtin_amdgcn_rcpf(1.0f + __builtin_amdgcn_exp2f(-1.4426950408889634f * x)); }
; __device__ __forceinline__ u32x4 pack8(const float (&v)[8]) { u32x4 w; w.x = pk2(v[0], v[1]); w.y = pk2(v[2], v[3]); w.z = pk2(v[4], v[5]); w.w = pk2(v[6], v[7]); return w; }
; __device__ __forceinline__ void ph_hgL(const Ctx& c) {
;     ...
;         const int bh = u >> 7, h = bh & 7;
;         if (u + c.G < 2048) HGL_DMA(u + c.G);
;         const float lbv = lb[h * 128 + d];
;         float cs[16], kk[16]; float run = 0.f;
; #pragma unroll
;         for (int i = 0; i < 16; ++i) { const float f = lbv + (1.0f - lbv) * sigmoidf_(bf2f(fl[i])); kk[i] = 1.0f - f; run += __builtin_amdgcn_logf(f); cs[i] = run; }
;         SS[seg * 128 + d] = run;
;         __syncthreads();
;         const float s0 = SS[d], s1 = SS[128 + d], s2 = SS[256 + d], s3 = SS[384 + d];
;         const float prefix = (seg > 0 ? s0 : 0.f) + (seg > 1 ? s1 : 0.f) + (seg > 2 ? s2 : 0.f), total = (s0 + s1) + (s2 + s3);
;         float kd[16];
; #pragma unroll
;         for (int i = 0; i < 16; ++i) kd[i] = kk[i] * __builtin_amdgcn_exp2f(total - prefix - cs[i]);
;         { float f0[8], f1[8];
; #pragma unroll
;           for (int i = 0; i < 8; ++i) { f0[i] = kd[i]; f1[i] = kd[8 + i]; }
;           *(LAS u32x4*)(KT + d * 72 + 16 * seg) = pack8(f0); *(LAS u32x4*)(KT + d * 72 + 16 * seg + 8) = pack8(f1);
;           *(LAS u32x4*)(VT + d * 72 + 16 * seg) = pk8us(vv[0], vv[1], vv[2], vv[3], vv[4], vv[5], vv[6], vv[7]);
;           *(LAS u32x4*)(VT + d * 72 + 16 * seg + 8) = pk8us(vv[8], vv[9], vv[10], vv[11], vv[12], vv[13], vv[14], vv[15]); }
;         if (seg == 0) DEC[(size_t)u * 128 + d] = __builtin_amdgcn_exp2f(total);
.LBB0_458:
	s_and_b32 s14, s34, 0x380
	v_lshlrev_b32_e32 v14, 16, v72
	v_lshlrev_b32_e32 v15, 16, v74
	v_lshlrev_b32_e32 v16, 16, v75
	v_mul_f32_e32 v14, 0xbfb8aa3b, v14
	v_mul_f32_e32 v15, 0xbfb8aa3b, v15
	v_mul_f32_e32 v16, 0xbfb8aa3b, v16
	v_exp_f32_e32 v14, v14
	v_exp_f32_e32 v15, v15
	v_exp_f32_e32 v16, v16
	v_lshlrev_b32_e32 v3, 16, v58
	v_lshlrev_b32_e32 v1, 16, v56
	v_lshlrev_b32_e32 v4, 16, v59
	v_mul_f32_e32 v3, 0xbfb8aa3b, v3
	v_lshlrev_b32_e32 v7, 16, v62
	v_lshlrev_b32_e32 v8, 16, v63
	v_mul_f32_e32 v1, 0xbfb8aa3b, v1
	v_mul_f32_e32 v4, 0xbfb8aa3b, v4
	v_exp_f32_e32 v3, v3
	v_lshlrev_b32_e32 v2, 16, v57
	v_lshlrev_b32_e32 v5, 16, v60
	v_lshlrev_b32_e32 v6, 16, v61
	v_lshlrev_b32_e32 v9, 16, v67
	v_lshlrev_b32_e32 v13, 16, v71
	v_mul_f32_e32 v7, 0xbfb8aa3b, v7
	v_mul_f32_e32 v8, 0xbfb8aa3b, v8
	v_exp_f32_e32 v1, v1
	v_exp_f32_e32 v4, v4
	v_add_f32_e32 v29, 1.0, v14
	v_add_f32_e32 v14, 1.0, v15
	v_add_f32_e32 v15, 1.0, v16
	v_lshlrev_b32_e32 v11, 16, v69
	v_lshlrev_b32_e32 v12, 16, v70
	v_mul_f32_e32 v2, 0xbfb8aa3b, v2
	v_mul_f32_e32 v5, 0xbfb8aa3b, v5
	v_mul_f32_e32 v6, 0xbfb8aa3b, v6
	v_mul_f32_e32 v9, 0xbfb8aa3b, v9
	v_mul_f32_e32 v13, 0xbfb8aa3b, v13
	v_exp_f32_e32 v7, v7
	v_exp_f32_e32 v8, v8
	v_rcp_f32_e32 v14, v14
	v_rcp_f32_e32 v15, v15
	v_lshlrev_b32_e32 v10, 16, v68
	v_mul_f32_e32 v11, 0xbfb8aa3b, v11
	v_mul_f32_e32 v12, 0xbfb8aa3b, v12
	v_exp_f32_e32 v2, v2
	v_exp_f32_e32 v5, v5
	v_exp_f32_e32 v6, v6
	v_exp_f32_e32 v9, v9
	v_exp_f32_e32 v13, v13
	v_mul_f32_e32 v10, 0xbfb8aa3b, v10
	v_exp_f32_e32 v11, v11
	v_exp_f32_e32 v12, v12
	v_add_f32_e32 v18, 1.0, v3
	v_exp_f32_e32 v10, v10
	v_add_f32_e32 v1, 1.0, v1
	v_add_f32_e32 v19, 1.0, v4
	v_rcp_f32_e32 v4, v18
	v_add_f32_e32 v22, 1.0, v7
	v_add_f32_e32 v23, 1.0, v8
	v_add_f32_e32 v17, 1.0, v2
	v_add_f32_e32 v20, 1.0, v5
	v_add_f32_e32 v21, 1.0, v6
	v_add_f32_e32 v24, 1.0, v9
	v_add_f32_e32 v28, 1.0, v13
	v_rcp_f32_e32 v5, v19
	v_rcp_f32_e32 v8, v22
	v_rcp_f32_e32 v9, v23
	v_add_f32_e32 v26, 1.0, v11
	v_add_f32_e32 v27, 1.0, v12
	v_rcp_f32_e32 v3, v17
	v_rcp_f32_e32 v6, v20
	v_rcp_f32_e32 v7, v21
	v_rcp_f32_e32 v16, v28
	v_rcp_f32_e32 v17, v29
	v_add_f32_e32 v25, 1.0, v10
	v_rcp_f32_e32 v12, v26
	v_rcp_f32_e32 v13, v27
	v_rcp_f32_e32 v2, v1
	v_rcp_f32_e32 v10, v24
	v_mov_b32_e32 v0, v102
	v_sub_f32_e32 v18, 1.0, v0
	v_pk_fma_f32 v[14:15], v[14:15], v[18:19], v[0:1] op_sel_hi:[1,0,0]
	v_rcp_f32_e32 v11, v25
	v_log_f32_e32 v19, v14
	v_pk_add_f32 v[20:21], v[14:15], 1.0 op_sel_hi:[1,0] neg_lo:[1,0] neg_hi:[1,0]
	v_log_f32_e32 v22, v15
	v_pk_fma_f32 v[8:9], v[8:9], v[18:19], v[0:1] op_sel_hi:[1,0,0]
	s_nop 0
	v_log_f32_e32 v23, v8
	v_pk_add_f32 v[14:15], v[8:9], 1.0 op_sel_hi:[1,0] neg_lo:[1,0] neg_hi:[1,0]
	v_log_f32_e32 v24, v9
	v_pk_fma_f32 v[8:9], v[16:17], v[18:19], v[0:1] op_sel_hi:[1,0,0]
	v_pk_fma_f32 v[6:7], v[6:7], v[18:19], v[0:1] op_sel_hi:[1,0,0]
	v_log_f32_e32 v25, v8
	v_pk_add_f32 v[16:17], v[8:9], 1.0 op_sel_hi:[1,0] neg_lo:[1,0] neg_hi:[1,0]
	v_log_f32_e32 v26, v9
	v_log_f32_e32 v27, v6
	v_pk_add_f32 v[8:9], v[6:7], 1.0 op_sel_hi:[1,0] neg_lo:[1,0] neg_hi:[1,0]
	v_log_f32_e32 v28, v7
	v_pk_fma_f32 v[6:7], v[12:13], v[18:19], v[0:1] op_sel_hi:[1,0,0]
	v_pk_fma_f32 v[4:5], v[4:5], v[18:19], v[0:1] op_sel_hi:[1,0,0]
	v_log_f32_e32 v29, v6
	v_pk_add_f32 v[12:13], v[6:7], 1.0 op_sel_hi:[1,0] neg_lo:[1,0] neg_hi:[1,0]
	v_log_f32_e32 v30, v7
	v_pk_fma_f32 v[6:7], v[10:11], v[18:19], v[0:1] op_sel_hi:[1,0,0]
	v_pk_fma_f32 v[0:1], v[2:3], v[18:19], v[0:1] op_sel_hi:[1,0,0]
	v_log_f32_e32 v31, v4
	v_log_f32_e32 v2, v0
	v_log_f32_e32 v3, v1
	v_log_f32_e32 v82, v5
	v_log_f32_e32 v10, v6
	v_add_f32_e32 v83, 0, v2
	v_add_f32_e32 v84, v3, v83
	v_add_f32_e32 v31, v31, v84
	v_add_f32_e32 v82, v82, v31
	v_add_f32_e32 v27, v27, v82
	v_log_f32_e32 v11, v7
	v_add_f32_e32 v28, v28, v27
	v_add_f32_e32 v85, v23, v28
	v_add_f32_e32 v86, v24, v85
	v_add_f32_e32 v87, v10, v86
	v_add_f32_e32 v88, v11, v87
	v_add_f32_e32 v29, v29, v88
	v_add_f32_e32 v30, v30, v29
	v_add_f32_e32 v89, v25, v30
	v_add_f32_e32 v26, v26, v89
	v_add_f32_e32 v90, v19, v26
	v_add_f32_e32 v91, v22, v90
	ds_write_b32 v64, v91 offset:36864
	s_waitcnt lgkmcnt(0)
	s_barrier
	ds_read2st64_b32 v[2:3], v65 offset0:144 offset1:146
	ds_read2st64_b32 v[10:11], v65 offset0:148 offset1:150
	v_pk_add_f32 v[18:19], v[0:1], 1.0 op_sel_hi:[1,0] neg_lo:[1,0] neg_hi:[1,0]
	v_pk_add_f32 v[4:5], v[4:5], 1.0 op_sel_hi:[1,0] neg_lo:[1,0] neg_hi:[1,0]
	v_pk_add_f32 v[6:7], v[6:7], 1.0 op_sel_hi:[1,0] neg_lo:[1,0] neg_hi:[1,0]
	s_waitcnt lgkmcnt(1)
	v_cndmask_b32_e64 v1, 0, v2, s[0:1]
	v_cndmask_b32_e64 v23, 0, v3, s[4:5]
	v_mov_b32_e32 v0, v2
	v_mov_b32_e32 v22, v3
	s_waitcnt lgkmcnt(0)
	v_cndmask_b32_e64 v25, 0, v10, s[6:7]
	v_add_f32_e32 v24, v10, v11
	v_pk_add_f32 v[0:1], v[0:1], v[22:23]
	s_nop 0
	v_pk_add_f32 v[0:1], v[0:1], v[24:25]
	s_nop 0
	v_sub_f32_e32 v1, v0, v1
	v_sub_f32_e32 v2, v1, v83
	v_sub_f32_e32 v3, v1, v84
	v_sub_f32_e32 v10, v1, v31
	v_sub_f32_e32 v11, v1, v82
	v_sub_f32_e32 v22, v1, v27
	v_sub_f32_e32 v23, v1, v28
	v_sub_f32_e32 v24, v1, v85
	v_sub_f32_e32 v25, v1, v86
	v_exp_f32_e32 v2, v2
	v_exp_f32_e32 v3, v3
	v_exp_f32_e32 v10, v10
	v_exp_f32_e32 v11, v11
	v_exp_f32_e32 v22, v22
	v_exp_f32_e32 v23, v23
	v_exp_f32_e32 v24, v24
	v_exp_f32_e32 v25, v25
	v_pk_mul_f32 v[2:3], v[18:19], v[2:3]
	v_pk_mul_f32 v[4:5], v[4:5], v[10:11]
	v_pk_mul_f32 v[8:9], v[8:9], v[22:23]
	v_pk_mul_f32 v[10:11], v[14:15], v[24:25]
	v_sub_f32_e32 v14, v1, v87
	v_sub_f32_e32 v15, v1, v88
	v_sub_f32_e32 v18, v1, v29
	v_sub_f32_e32 v19, v1, v30
	v_sub_f32_e32 v22, v1, v89
	v_sub_f32_e32 v23, v1, v26
	v_sub_f32_e32 v24, v1, v90
	v_sub_f32_e32 v1, v1, v91
	v_exp_f32_e32 v14, v14
	v_exp_f32_e32 v15, v15
	v_exp_f32_e32 v18, v18
	v_exp_f32_e32 v19, v19
	v_exp_f32_e32 v22, v22
	v_exp_f32_e32 v23, v23
	v_exp_f32_e32 v24, v24
	v_exp_f32_e32 v25, v1
	v_pk_mul_f32 v[6:7], v[6:7], v[14:15]
	v_pk_mul_f32 v[12:13], v[12:13], v[18:19]
	v_pk_mul_f32 v[14:15], v[16:17], v[22:23]
	v_pk_mul_f32 v[16:17], v[20:21], v[24:25]
	v_cvt_pk_bf16_f32 v2, v2, v3
	v_cvt_pk_bf16_f32 v3, v4, v5
	v_cvt_pk_bf16_f32 v4, v8, v9
	v_cvt_pk_bf16_f32 v5, v10, v11
	ds_write_b128 v66, v[2:5] offset:18432
	v_cvt_pk_bf16_f32 v2, v6, v7
	v_cvt_pk_bf16_f32 v3, v12, v13
	v_cvt_pk_bf16_f32 v4, v14, v15
	v_cvt_pk_bf16_f32 v5, v16, v17
	ds_write_b128 v66, v[2:5] offset:18448
	ds_write_b128 v66, v[36:39]
	ds_write_b128 v66, v[32:35] offset:16
	s_and_saveexec_b64 s[34:35], s[8:9]
	s_cbranch_execz .LBB0_460
	v_exp_f32_e32 v2, v0
	v_lshl_add_u64 v[0:1], s[46:47], 0, v[44:45]
	global_store_dword v[0:1], v2, off
; #define LAS __attribute__((address_space(3)))
; #define HGL_COLS() do { asm volatile("s_waitcnt vmcnt(0)" ::: "memory"); _Pragma("unroll") for (int i = 0; i < 16; ++i) { fl[i] = *(const LAS unsigned short*)(ZW + i * 128 + c.lane * 2); vv[i] = *(const LAS unsigned short*)(ZW + 2048 + i * 128 + c.lane * 2); } \
;         asm volatile("s_waitcnt lgkmcnt(0)" ::: "memory"); } while (0)
; __device__ __forceinline__ void ph_hgL(const Ctx& c) {
;     ...
;         const int vdt = w >> 1, kdt0 = (w & 1) * 2;
;         f32x16 acc0, acc1;
; #pragma unroll
;         for (int i = 0; i < 16; ++i) { acc0[i] = 0.f; acc1[i] = 0.f; }
; #pragma unroll
;         for (int ks = 0; ks < 4; ++ks) {
;             const bf16x8 a = *(const LAS bf16x8*)(VT + (32 * vdt + r) * 72 + 16 * ks + 8 * hh);
;             const bf16x8 b0 = *(const LAS bf16x8*)(KT + (32 * kdt0 + r) * 72 + 16 * ks + 8 * hh), b1 = *(const LAS bf16x8*)(KT + (32 * (kdt0 + 1) + r) * 72 + 16 * ks + 8 * hh);
;             acc0 = __builtin_amdgcn_mfma_f32_32x32x16_bf16(a, b0, acc0, 0, 0, 0); acc1 = __builtin_amdgcn_mfma_f32_32x32x16_bf16(a, b1, acc1, 0, 0, 0);
;         }
;         bf16* kvp = (bf16*)KV + (size_t)u * 16384;
; #pragma unroll
;         for (int i = 0; i < 16; ++i) { const int vd = 32 * vdt + (i & 3) + 8 * (i >> 2) + 4 * hh; ST[vd * 136 + 32 * kdt0 + r] = f2bf(acc0[i]); ST[vd * 136 + 32 * (kdt0 + 1) + r] = f2bf(acc1[i]); }
;         __syncthreads();
;         if (u + c.G < 2048) HGL_COLS();
.LBB0_460:
	s_or_b64 exec, exec, s[34:35]
	s_waitcnt lgkmcnt(0)
	s_barrier
	ds_read_b128 v[16:19], v73
	ds_read_b128 v[0:3], v76 offset:18432
	ds_read_b128 v[82:85], v73 offset:32
	ds_read_b128 v[86:89], v76 offset:18464
	s_waitcnt lgkmcnt(2)
	v_mfma_f32_32x32x16_bf16 v[0:15], v[16:19], v[0:3], 0
	ds_read_b128 v[20:23], v76 offset:23040
	ds_read_b128 v[90:93], v76 offset:23072
	s_andn2_b64 vcc, exec, s[30:31]
	s_waitcnt lgkmcnt(1)
	v_mfma_f32_32x32x16_bf16 v[16:31], v[16:19], v[20:23], 0
	v_mfma_f32_32x32x16_bf16 v[0:15], v[82:85], v[86:89], v[0:15]
	s_waitcnt lgkmcnt(0)
	v_mfma_f32_32x32x16_bf16 v[16:31], v[82:85], v[90:93], v[16:31]
	ds_read_b128 v[82:85], v73 offset:64
	ds_read_b128 v[86:89], v76 offset:18496
	ds_read_b128 v[90:93], v73 offset:96
	ds_read_b128 v[94:97], v76 offset:18528
	s_waitcnt lgkmcnt(2)
	v_mfma_f32_32x32x16_bf16 v[0:15], v[82:85], v[86:89], v[0:15]
	ds_read_b128 v[86:89], v76 offset:23104
	ds_read_b128 v[98:101], v76 offset:23136
	s_waitcnt lgkmcnt(1)
	v_mfma_f32_32x32x16_bf16 v[16:31], v[82:85], v[86:89], v[16:31]
	v_mfma_f32_32x32x16_bf16 v[0:15], v[90:93], v[94:97], v[0:15]
	s_waitcnt lgkmcnt(0)
	v_mfma_f32_32x32x16_bf16 v[16:31], v[90:93], v[98:101], v[16:31]
	s_nop 9
	v_cvt_pk_bf16_f32 v0, v0, s0
	ds_write_b16 v77, v0
	v_cvt_pk_bf16_f32 v0, v16, s0
	ds_write_b16 v77, v0 offset:64
	v_cvt_pk_bf16_f32 v0, v1, s0
	ds_write_b16 v77, v0 offset:272
	v_cvt_pk_bf16_f32 v0, v17, s0
	ds_write_b16 v77, v0 offset:336
	v_cvt_pk_bf16_f32 v0, v2, s0
	ds_write_b16 v77, v0 offset:544
	v_cvt_pk_bf16_f32 v0, v18, s0
	ds_write_b16 v77, v0 offset:608
	v_cvt_pk_bf16_f32 v0, v3, s0
	ds_write_b16 v77, v0 offset:816
	v_cvt_pk_bf16_f32 v0, v19, s0
	ds_write_b16 v77, v0 offset:880
	v_cvt_pk_bf16_f32 v0, v4, s0
	ds_write_b16 v77, v0 offset:2176
	v_cvt_pk_bf16_f32 v0, v20, s0
	ds_write_b16 v77, v0 offset:2240
	v_cvt_pk_bf16_f32 v0, v5, s0
	ds_write_b16 v77, v0 offset:2448
	v_cvt_pk_bf16_f32 v0, v21, s0
	ds_write_b16 v77, v0 offset:2512
	v_cvt_pk_bf16_f32 v0, v6, s0
	ds_write_b16 v77, v0 offset:2720
	v_cvt_pk_bf16_f32 v0, v22, s0
	ds_write_b16 v77, v0 offset:2784
	v_cvt_pk_bf16_f32 v0, v7, s0
	ds_write_b16 v77, v0 offset:2992
	v_cvt_pk_bf16_f32 v0, v23, s0
	ds_write_b16 v77, v0 offset:3056
	v_cvt_pk_bf16_f32 v0, v8, s0
	ds_write_b16 v77, v0 offset:4352
	v_cvt_pk_bf16_f32 v0, v24, s0
	ds_write_b16 v77, v0 offset:4416
	v_cvt_pk_bf16_f32 v0, v9, s0
	ds_write_b16 v77, v0 offset:4624
	v_cvt_pk_bf16_f32 v0, v25, s0
	ds_write_b16 v77, v0 offset:4688
	v_cvt_pk_bf16_f32 v0, v10, s0
	ds_write_b16 v77, v0 offset:4896
	v_cvt_pk_bf16_f32 v0, v26, s0
	ds_write_b16 v77, v0 offset:4960
	v_cvt_pk_bf16_f32 v0, v11, s0
	ds_write_b16 v77, v0 offset:5168
	v_cvt_pk_bf16_f32 v0, v27, s0
	ds_write_b16 v77, v0 offset:5232
	v_cvt_pk_bf16_f32 v0, v12, s0
	ds_write_b16 v77, v0 offset:6528
	v_cvt_pk_bf16_f32 v0, v28, s0
	ds_write_b16 v77, v0 offset:6592
	v_cvt_pk_bf16_f32 v0, v13, s0
	ds_write_b16 v77, v0 offset:6800
	v_cvt_pk_bf16_f32 v0, v29, s0
	ds_write_b16 v77, v0 offset:6864
	v_cvt_pk_bf16_f32 v0, v14, s0
	ds_write_b16 v77, v0 offset:7072
	v_cvt_pk_bf16_f32 v0, v30, s0
	ds_write_b16 v77, v0 offset:7136
	v_cvt_pk_bf16_f32 v0, v15, s0
	ds_write_b16 v77, v0 offset:7344
	v_cvt_pk_bf16_f32 v0, v31, s0
	ds_write_b16 v77, v0 offset:7408
	s_waitcnt lgkmcnt(0)
	s_barrier
	s_cbranch_vccnz .LBB0_455
	v_mov_b32_e32 v102, s41
	v_and_b32_e32 v102, 0x380, v102
	v_or_b32_e32 v102, v102, v54
	v_lshlrev_b32_e32 v102, 2, v102
	global_load_dword v102, v102, s[12:13]
	s_waitcnt vmcnt(0)
	ds_read_u16 v56, v55
	ds_read_u16 v57, v55 offset:128
	ds_read_u16 v58, v55 offset:256
	ds_read_u16 v59, v55 offset:384
	ds_read_u16 v60, v55 offset:512
	ds_read_u16 v61, v55 offset:640
	ds_read_u16 v62, v55 offset:768
	ds_read_u16 v63, v55 offset:896
	ds_read_u16 v0, v55 offset:2048
	ds_read_u16 v1, v55 offset:2176
	ds_read_u16 v2, v55 offset:2304
	ds_read_u16 v3, v55 offset:2432
	ds_read_u16 v4, v55 offset:2560
	ds_read_u16 v5, v55 offset:2688
	ds_read_u16 v6, v55 offset:2816
	ds_read_u16 v7, v55 offset:2944
	ds_read_u16 v8, v55 offset:3072
	ds_read_u16 v9, v55 offset:3200
	ds_read_u16 v10, v55 offset:3328
	ds_read_u16 v11, v55 offset:3456
	ds_read_u16 v12, v55 offset:3584
	ds_read_u16 v13, v55 offset:3712
	ds_read_u16 v14, v55 offset:3840
	ds_read_u16 v15, v55 offset:3968
	ds_read_u16 v67, v55 offset:1024
	ds_read_u16 v68, v55 offset:1152
	ds_read_u16 v69, v55 offset:1280
	ds_read_u16 v70, v55 offset:1408
	ds_read_u16 v71, v55 offset:1536
	ds_read_u16 v72, v55 offset:1664
	ds_read_u16 v74, v55 offset:1792
	ds_read_u16 v75, v55 offset:1920
	s_waitcnt lgkmcnt(0)
	s_waitcnt lgkmcnt(8)
	v_perm_b32 v35, v15, v14, s36
	v_perm_b32 v34, v13, v12, s36
	v_perm_b32 v33, v11, v10, s36
	v_perm_b32 v32, v9, v8, s36
	v_perm_b32 v39, v7, v6, s36
	v_perm_b32 v38, v5, v4, s36
	v_perm_b32 v37, v3, v2, s36
	v_perm_b32 v36, v1, v0, s36
	s_branch .LBB0_455

; #define LAS __attribute__((address_space(3)))
; #define HGO_LOAD_G(U) do { const int _c = (U) & 127, _bh = (U) >> 7; \
;         const bf16* _gp = ZH + 3 * ZH_AS + ((size_t)_bh * SEQ + _c * 64 + ot) * 128 + ovd0; gn0 = *(const u32x4*)_gp; gn1 = *(const u32x4*)(_gp + 64); } while (0)
; #define HGO_LOAD_S(U) do { const bf16* _sp = SIN + (size_t)(U) * 16384 + (32 * vdt + r) * 128 + 8 * hh; _Pragma("unroll") for (int k8 = 0; k8 < 8; ++k8) sfr[k8] = *(const bf16x8*)(_sp + 16 * k8); } while (0)
; __device__ __forceinline__ void ph_hgO(const Ctx& c) {
;     const bf16* ZH = WSP(bf16, WS_XB); bf16* Y = WSP(bf16, WS_YCAT); const float* lb = WSP(float, WS_LB); const bf16* SIN = WSP(bf16, WS_SIN); const float* ng = c.in[7];
;     LAS bf16* QB = (LAS bf16*)c.lds; LAS bf16* QS = QB + 64 * 136; LAS bf16* KS = QS + 64 * 136; LAS bf16* VT = KS + 64 * 136;
;     LAS float* SS = (LAS float*)(c.lds + MISC_OFF + 1024); LAS float* RS = SS + 512; LAS float* OT = (LAS float*)(VT + 128 * 72);
;     const int d = c.tid & 127, seg = c.tid >> 7, r = c.lane & 31, hh = c.lane >> 5, w = c.wave, vdt = w & 3, tt = w >> 2;
;     bf16x8 sfr[8]; unsigned short fl[16], qq[16], vv[16]; u32x4 gn0, gn1;
;     const int ot = c.tid >> 3, ovd0 = (c.tid & 7) * 8;
;     LAS unsigned char* ZW = c.lds + 104448 + w * 6144;
;     const int zr = c.lane >> 3, zp = c.lane & 7;
;     ...
;     if (c.bid < 2048) { HGO_DMA(c.bid); HGO_LOAD_G(c.bid); HGO_LOAD_S(c.bid); HGO_COLS(0); }
.LBB0_567:
	v_readlane_b32 s0, v254, 5
	v_readlane_b32 s1, v254, 6
	s_cmp_lt_i32 s0, 5
	s_cselect_b64 s[0:1], -1, 0
	s_and_b64 s[58:59], s[0:1], s[4:5]
	s_andn2_b64 vcc, exec, s[58:59]
	s_cbranch_vccnz .LBB0_583
	s_cmpk_gt_i32 s2, 0x7ff
	s_cbranch_scc1 .LBB0_583
	v_readlane_b32 s41, v254, 46
	s_add_u32 s60, s46, 0x66b00000
	s_mul_i32 s0, s41, 0x1800
	s_addc_u32 s61, s47, 0
	v_readlane_b32 s5, v254, 4
	s_add_i32 s3, s0, 0
	s_lshr_b32 s33, s5, 8
	s_add_i32 s88, s3, 0x19800
	s_bfe_u32 s38, s5, 0x20006
	s_add_u32 s8, s46, 0x6d300000
	s_addc_u32 s9, s47, 0
	s_add_u32 s6, s46, 0x43500000
	v_ashrrev_i32_e32 v4, 3, v2
	v_ashrrev_i32_e32 v13, 7, v3
	s_addc_u32 s7, s47, 0
	s_ashr_i32 s0, s2, 7
	s_ashr_i32 s1, s0, 31
	s_lshl_b32 s4, s2, 6
	v_lshl_add_u32 v122, v13, 4, v4
	s_mov_b32 s67, 0
	s_and_b32 s66, s4, 0x1fc0
	v_ashrrev_i32_e32 v123, 31, v122
	s_lshl_b64 s[10:11], s[0:1], 21
	v_lshl_add_u64 v[4:5], s[66:67], 0, v[122:123]
	s_add_u32 s0, s6, s10
	v_lshlrev_b64 v[4:5], 8, v[4:5]
	s_addc_u32 s1, s7, s11
	v_lshl_add_u64 v[4:5], s[0:1], 0, v[4:5]
	s_and_b32 s0, s5, 64
	v_and_b32_e32 v6, 7, v2
	s_lshl_b32 s0, s0, 1
	s_mov_b32 s1, s67
	v_lshl_add_u64 v[4:5], v[4:5], 0, s[0:1]
	v_lshlrev_b32_e32 v124, 4, v6
	v_mov_b32_e32 v125, 0
	v_lshl_add_u64 v[4:5], v[4:5], 0, v[124:125]
	s_mov_b64 s[54:55], 0x2000000
	v_lshl_add_u64 v[6:7], v[4:5], 0, s[54:55]
	s_mov_b32 m0, s88
	s_mov_b64 s[56:57], 0x2000800
	global_load_lds_dwordx4 v[6:7], off
	v_lshl_add_u64 v[6:7], v[4:5], 0, s[56:57]
	s_add_i32 m0, s3, 0x19c00
	s_mov_b64 s[48:49], 0x800
	global_load_lds_dwordx4 v[6:7], off
	s_add_i32 m0, s3, 0x1a000
	v_lshl_add_u64 v[6:7], v[4:5], 0, s[48:49]
	global_load_lds_dwordx4 v[4:5], off
	s_add_i32 m0, s3, 0x1a400
	s_mov_b64 s[50:51], 0x4000000
	global_load_lds_dwordx4 v[6:7], off
	v_lshl_add_u64 v[6:7], v[4:5], 0, s[50:51]
	s_add_i32 m0, s3, 0x1a800
	v_ashrrev_i32_e32 v120, 3, v3
	global_load_lds_dwordx4 v[6:7], off
	s_add_i32 m0, s3, 0x1ac00
	s_mov_b64 s[52:53], 0x4000800
	s_add_u32 s4, s46, 0x49500000
	v_lshl_add_u64 v[4:5], v[4:5], 0, s[52:53]
	s_addc_u32 s5, s47, 0
	v_ashrrev_i32_e32 v121, 31, v120
	v_lshlrev_b32_e32 v0, 3, v2
	global_load_lds_dwordx4 v[4:5], off
	v_lshl_add_u64 v[4:5], s[66:67], 0, v[120:121]
	s_add_u32 s10, s4, s10
	v_and_b32_e32 v0, 56, v0
	v_lshlrev_b64 v[4:5], 8, v[4:5]
	s_addc_u32 s11, s5, s11
	v_lshl_add_u64 v[4:5], s[10:11], 0, v[4:5]
	v_lshlrev_b32_e32 v6, 1, v0
	v_mov_b32_e32 v7, v125
	s_ashr_i32 s3, s2, 31
	v_and_b32_e32 v1, 31, v2
	v_ashrrev_i32_e32 v12, 5, v2
	v_lshl_add_u64 v[4:5], v[4:5], 0, v[6:7]
	s_lshl_b64 s[10:11], s[2:3], 15
	global_load_dwordx4 v[76:79], v[4:5], off
	global_load_dwordx4 v[72:75], v[4:5], off offset:128
	s_add_u32 s10, s8, s10
	v_lshlrev_b32_e32 v4, 8, v1
	v_lshlrev_b32_e32 v10, 3, v12
	s_addc_u32 s11, s9, s11
	v_lshl_or_b32 v4, s38, 13, v4
	v_mov_b32_e32 v5, v125
	v_ashrrev_i32_e32 v11, 31, v10
	v_lshl_add_u64 v[8:9], s[10:11], 0, v[4:5]
	v_lshlrev_b64 v[10:11], 1, v[10:11]
	v_lshl_add_u64 v[8:9], v[8:9], 0, v[10:11]
	global_load_dwordx4 v[40:43], v[8:9], off
	global_load_dwordx4 v[44:47], v[8:9], off offset:32
	global_load_dwordx4 v[48:51], v[8:9], off offset:64
	global_load_dwordx4 v[52:55], v[8:9], off offset:96
	global_load_dwordx4 v[56:59], v[8:9], off offset:128
	global_load_dwordx4 v[60:63], v[8:9], off offset:160
	global_load_dwordx4 v[64:67], v[8:9], off offset:192
	global_load_dwordx4 v[68:71], v[8:9], off offset:224
	s_add_i32 s39, 0, 0x11400
	s_add_i32 s40, 0, 0x26c00
	s_add_u32 s0, s6, s0
	s_waitcnt vmcnt(0)
	v_lshl_add_u32 v135, v2, 1, s88
	s_addc_u32 s1, s7, 0
	ds_read_u16 v136, v135
	ds_read_u16 v137, v135 offset:128
	ds_read_u16 v138, v135 offset:256
	ds_read_u16 v139, v135 offset:384
	ds_read_u16 v140, v135 offset:512
	ds_read_u16 v141, v135 offset:640
	ds_read_u16 v142, v135 offset:768
	ds_read_u16 v143, v135 offset:896
	ds_read_u16 v144, v135 offset:2048
	ds_read_u16 v145, v135 offset:2176
	ds_read_u16 v146, v135 offset:2304
	ds_read_u16 v147, v135 offset:2432
	ds_read_u16 v148, v135 offset:2560
	ds_read_u16 v149, v135 offset:2688
	ds_read_u16 v150, v135 offset:2816
	ds_read_u16 v151, v135 offset:2944
	ds_read_u16 v14, v135 offset:4096
	ds_read_u16 v15, v135 offset:4224
	ds_read_u16 v8, v135 offset:4352
	ds_read_u16 v9, v135 offset:4480
	ds_read_u16 v16, v135 offset:4608
	ds_read_u16 v17, v135 offset:4736
	ds_read_u16 v18, v135 offset:4864
	ds_read_u16 v19, v135 offset:4992
	ds_read_u16 v152, v135 offset:1024
	ds_read_u16 v153, v135 offset:1152
	ds_read_u16 v154, v135 offset:1280
	ds_read_u16 v155, v135 offset:1408
	ds_read_u16 v156, v135 offset:1536
	ds_read_u16 v158, v135 offset:1664
	ds_read_u16 v160, v135 offset:1792
	ds_read_u16 v161, v135 offset:1920
	ds_read_u16 v20, v135 offset:5120
	ds_read_u16 v21, v135 offset:5248
	ds_read_u16 v22, v135 offset:5376
	ds_read_u16 v23, v135 offset:5504
	ds_read_u16 v24, v135 offset:5632
	ds_read_u16 v25, v135 offset:5760
	ds_read_u16 v26, v135 offset:5888
	ds_read_u16 v27, v135 offset:6016
	ds_read_u16 v162, v135 offset:3072
	ds_read_u16 v163, v135 offset:3200
	ds_read_u16 v164, v135 offset:3328
	ds_read_u16 v165, v135 offset:3456
	ds_read_u16 v167, v135 offset:3584
	ds_read_u16 v168, v135 offset:3712
	ds_read_u16 v169, v135 offset:3840
	ds_read_u16 v170, v135 offset:3968
	s_mov_b32 s3, 0x5040100
	v_lshl_add_u64 v[126:127], s[0:1], 0, v[124:125]
	s_add_i32 s0, 0, 0x26400
	v_and_b32_e32 v134, 0x7f, v3
	s_waitcnt lgkmcnt(0)
; #define LAS __attribute__((address_space(3)))
; __device__ __forceinline__ float bf2f(bf16 b) { return __uint_as_float(((unsigned)b) << 16); }
; __device__ __forceinline__ float sigmoidf_(float x) { return __builtin_amdgcn_rcpf(1.0f + __builtin_amdgcn_exp2f(-1.4426950408889634f * x)); }
; #define HGO_LOAD_G(U) do { const int _c = (U) & 127, _bh = (U) >> 7; \
;         const bf16* _gp = ZH + 3 * ZH_AS + ((size_t)_bh * SEQ + _c * 64 + ot) * 128 + ovd0; gn0 = *(const u32x4*)_gp; gn1 = *(const u32x4*)(_gp + 64); } while (0)
; __device__ __forceinline__ void ph_hgO(const Ctx& c) {
;     ...
;     if (c.bid < 2048) { HGO_DMA(c.bid); HGO_LOAD_G(c.bid); HGO_LOAD_S(c.bid); HGO_COLS(0); }
;     for (int u = c.bid; u < 2048; u += c.G) {
;         const int chunk = u & 127, bh = u >> 7, h = bh & 7, b = bh >> 3; const int t0 = b * SEQ + chunk * 64;
;         const u32x4 gc0 = gn0, gc1 = gn1;
;         if (u + c.G < 2048) { HGO_DMA(u + c.G); HGO_LOAD_G(u + c.G); }
;         const float lbv = lb[h * 128 + d];
;         float cs[16], kk[16]; float run = 0.f;
; #pragma unroll
;         for (int i = 0; i < 16; ++i) { const float f = lbv + (1.0f - lbv) * sigmoidf_(bf2f(fl[i])); kk[i] = 1.0f - f; run += __builtin_amdgcn_logf(f); cs[i] = run; }
;         SS[seg * 128 + d] = run;
;         __syncthreads();
;         { const float s0 = SS[d], s1 = SS[128 + d], s2 = SS[256 + d];
;           const float prefix = (seg > 0 ? s0 : 0.f) + (seg > 1 ? s1 : 0.f) + (seg > 2 ? s2 : 0.f), ref = s0 + s1;
; #pragma unroll
;           for (int i = 0; i < 16; ++i) { const float bb = prefix + cs[i], q = bf2f(qq[i]); const int t = 16 * seg + i;
;               QB[t * 136 + d] = f2bf(q * __builtin_amdgcn_exp2f(bb)); QS[t * 136 + d] = f2bf(q * __builtin_amdgcn_exp2f(bb - ref)); KS[t * 136 + d] = f2bf(kk[i] * __builtin_amdgcn_exp2f(ref - bb)); }
;           *(LAS u32x4*)(VT + d * 72 + 16 * seg) = pk8us(vv[0], vv[1], vv[2], vv[3], vv[8], vv[9], vv[10], vv[11]);
;           *(LAS u32x4*)(VT + d * 72 + 16 * seg + 8) = pk8us(vv[4], vv[5], vv[6], vv[7], vv[12], vv[13], vv[14], vv[15]); }
;     ...
;             if (st == tt) {
; #pragma unroll
;                 for (int i = 0; i < 16; ++i) { const int row = (i & 3) + 8 * (i >> 2) + 4 * hh; if (row > r) x[i] = 0.f; }
	v_perm_b32 v36, v17, v16, s3
	v_lshl_add_u32 v17, v2, 2, s40
	v_lshl_add_u32 v157, v3, 2, s0
	v_lshl_add_u64 v[4:5], s[8:9], 0, v[4:5]
	v_cmp_gt_u32_e64 s[8:9], 32, v2
	v_lshlrev_b32_e32 v2, 1, v3
	v_lshlrev_b32_e32 v3, 2, v120
	s_movk_i32 s10, 0x90
	v_lshl_add_u64 v[130:131], v[4:5], 0, v[10:11]
	v_lshlrev_b32_e32 v11, 2, v12
	v_and_b32_e32 v2, 0xfffffe00, v2
	v_and_b32_e32 v3, 0x7c, v3
	v_perm_b32 v39, v9, v8, s3
	v_lshl_add_u64 v[128:129], s[4:5], 0, v[6:7]
	v_mad_u32_u24 v6, v134, s10, 0
	v_lshl_or_b32 v9, s33, 5, v1
	s_movk_i32 s10, 0x110
	v_add3_u32 v166, s40, v2, v3
	v_or_b32_e32 v2, v2, v3
	v_or_b32_e32 v3, 2, v11
	v_perm_b32 v37, v19, v18, s3
	v_mul_lo_u32 v18, v9, s10
	v_cmp_gt_i32_e64 s[10:11], v3, v1
	v_or_b32_e32 v3, 3, v11
	v_cmp_gt_i32_e64 s[12:13], v3, v1
	v_add_u32_e32 v3, 8, v11
	v_cmp_gt_i32_e64 s[14:15], v3, v1
	v_add_u32_e32 v3, 9, v11
	v_cmp_gt_i32_e64 s[16:17], v3, v1
	v_add_u32_e32 v3, 10, v11
	v_cmp_gt_i32_e64 s[18:19], v3, v1
	v_add_u32_e32 v3, 11, v11
	v_cmp_gt_i32_e64 s[20:21], v3, v1
	v_add_u32_e32 v3, 16, v11
	v_cmp_gt_i32_e64 s[22:23], v3, v1
	v_add_u32_e32 v3, 17, v11
	v_mbcnt_lo_u32_b32 v4, -1, 0
	v_cmp_gt_i32_e64 s[24:25], v3, v1
	v_add_u32_e32 v3, 18, v11
	v_mbcnt_hi_u32_b32 v4, -1, v4
	v_cmp_gt_i32_e64 s[26:27], v3, v1
	v_add_u32_e32 v3, 19, v11
	v_and_b32_e32 v10, 64, v4
	v_cmp_gt_i32_e64 s[28:29], v3, v1
	v_add_u32_e32 v3, 24, v11
	v_xor_b32_e32 v5, 32, v4
	v_add_u32_e32 v10, 64, v10
	v_cmp_gt_i32_e64 s[30:31], v3, v1
	v_add_u32_e32 v3, 25, v11
	v_cmp_lt_i32_e32 vcc, v5, v10
	v_cmp_gt_i32_e64 s[34:35], v3, v1
	v_add_u32_e32 v3, 26, v11
	v_add_u32_e32 v2, s40, v2
	v_cndmask_b32_e32 v4, v4, v5, vcc
	v_cmp_gt_i32_e64 s[36:37], v3, v1
	v_lshl_or_b32 v3, s38, 5, v1
	s_movk_i32 s45, 0x210
	s_lshl_b32 s38, s38, 7
	v_add_u32_e32 v172, 0x180, v2
	v_add_u32_e32 v2, 27, v11
	v_lshlrev_b32_e32 v8, 2, v0
	v_lshlrev_b32_e32 v171, 2, v4
	v_mul_lo_u32 v4, v9, s45
	s_add_i32 s38, s38, s39
	v_cmp_gt_i32_e64 s[42:43], v2, v1
	v_mul_lo_u32 v2, v120, s45
	s_movk_i32 s45, 0x880
	s_waitcnt lgkmcnt(0)
	v_add_u32_e32 v16, s39, v8
	v_lshlrev_b32_e32 v10, 4, v12
	v_mul_u32_u24_e32 v3, 0x90, v3
	s_lshl_b32 s44, s41, 7
	v_add_u32_e32 v4, s38, v4
	v_cmp_gt_i32_e64 s[38:39], v11, v1
	v_cmp_lt_i32_e64 s[40:41], v11, v1
	v_mul_lo_u32 v5, v13, s45
	v_readlane_b32 s68, v254, 11
	v_mul_u32_u24_e32 v1, 0x110, v1
	v_lshlrev_b32_e32 v7, 5, v13
	v_add_u32_e32 v18, 0, v18
	v_or_b32_e32 v5, v5, v134
	v_mov_b32_e32 v9, v125
	v_readlane_b32 s69, v254, 12
	v_readlane_b32 s70, v254, 13
	v_readlane_b32 s82, v254, 25
	v_readlane_b32 s83, v254, 26
	v_add3_u32 v3, v3, v10, 0
	v_add3_u32 v1, v1, v10, 0
	s_waitcnt vmcnt(0)
	v_mov_b64_e32 v[82:83], v[74:75]
	v_mov_b64_e32 v[86:87], v[78:79]
	v_perm_b32 v33, v27, v26, s3
	v_perm_b32 v32, v25, v24, s3
	v_perm_b32 v35, v23, v22, s3
	v_perm_b32 v34, v21, v20, s3
	v_lshl_add_u32 v159, v134, 2, s0
	v_cmp_lt_i32_e64 s[0:1], 0, v13
	v_cmp_lt_i32_e64 s[4:5], 1, v13
	v_cmp_lt_i32_e64 s[6:7], 2, v13
	v_lshl_add_u32 v173, v5, 1, 0
	v_lshl_add_u64 v[132:133], s[82:83], 0, v[8:9]
	v_add_u32_e32 v174, 0xcc00, v3
	s_sub_i32 s89, 0, s33
	v_add_u32_e32 v175, 0x8800, v1
	s_add_i32 s97, s88, 0x400
	s_add_i32 s33, s88, 0xc00
	s_add_i32 s68, s88, 0x1000
	s_add_i32 s69, s88, 0x1400
	v_add_u32_e32 v176, v6, v7
	v_add_u32_e32 v177, s44, v17
	v_add_u32_e32 v178, v4, v10
	v_mov_b32_e32 v179, 0x358637bd
	v_lshlrev_b32_e32 v124, 1, v0
	v_add_u32_e32 v180, v16, v2
	v_add_u32_e32 v181, v18, v10
	s_mov_b32 s70, s2
	v_mov_b64_e32 v[80:81], v[72:73]
	v_mov_b64_e32 v[84:85], v[76:77]
	v_perm_b32 v38, v15, v14, s3
	v_readlane_b32 s71, v254, 14
	v_readlane_b32 s72, v254, 15
	v_readlane_b32 s73, v254, 16
	v_readlane_b32 s74, v254, 17
	v_readlane_b32 s75, v254, 18
	v_readlane_b32 s76, v254, 19
	v_readlane_b32 s77, v254, 20
	v_readlane_b32 s78, v254, 21
	v_readlane_b32 s79, v254, 22
	v_readlane_b32 s80, v254, 23
	v_readlane_b32 s81, v254, 24
	v_mov_b32_e32 v188, s70
	v_and_b32_e32 v188, 0x380, v188
	v_or_b32_e32 v188, v188, v134
	v_lshlrev_b32_e32 v188, 2, v188
	global_load_dword v188, v188, s[60:61]
	s_waitcnt vmcnt(0)
	s_branch .LBB0_571
; #define LAS __attribute__((address_space(3)))
; __device__ __forceinline__ float siluf_(float x) { return x * __builtin_amdgcn_rcpf(1.0f + __builtin_amdgcn_exp2f(-1.4426950408889634f * x)); }
; __device__ __forceinline__ u32x4 pack8(const float (&v)[8]) { u32x4 w; w.x = pk2(v[0], v[1]); w.y = pk2(v[2], v[3]); w.z = pk2(v[4], v[5]); w.w = pk2(v[6], v[7]); return w; }
; #define HGO_LOAD_G(U) do { const int _c = (U) & 127, _bh = (U) >> 7; \
;         const bf16* _gp = ZH + 3 * ZH_AS + ((size_t)_bh * SEQ + _c * 64 + ot) * 128 + ovd0; gn0 = *(const u32x4*)_gp; gn1 = *(const u32x4*)(_gp + 64); } while (0)
; __device__ __forceinline__ void ph_hgO(const Ctx& c) {
;     ...
;         const int chunk = u & 127, bh = u >> 7, h = bh & 7, b = bh >> 3; const int t0 = b * SEQ + chunk * 64;
;         const u32x4 gc0 = gn0, gc1 = gn1;
;         if (u + c.G < 2048) { HGO_DMA(u + c.G); HGO_LOAD_G(u + c.G); }
;         const float lbv = lb[h * 128 + d];
;     ...
;         { const int t = ot, vd0 = ovd0;
;           const float ssum = (RS[((t >> 5) * 4 + 0) * 32 + (t & 31)] + RS[((t >> 5) * 4 + 1) * 32 + (t & 31)]) + (RS[((t >> 5) * 4 + 2) * 32 + (t & 31)] + RS[((t >> 5) * 4 + 3) * 32 + (t & 31)]);
;           const float rr = rsqrtf(ssum * (1.0f / 128.0f) + EPS);
; #pragma unroll
;           for (int hf = 0; hf < 2; ++hf) { float g[8], o[8]; unpack8(hf ? gc1 : gc0, g);
;               const f32x4 oa = *(const LAS f32x4*)(OT + t * 132 + vd0 + 64 * hf), ob = *(const LAS f32x4*)(OT + t * 132 + vd0 + 64 * hf + 4);
; #pragma unroll
;               for (int j = 0; j < 4; ++j) { o[j] = oa[j] * rr * ng[vd0 + 64 * hf + j] * siluf_(g[j]); o[4 + j] = ob[j] * rr * ng[vd0 + 64 * hf + 4 + j] * siluf_(g[4 + j]); }
;               *(u32x4*)(Y + (size_t)(t0 + t) * D_ + 1024 + h * 128 + vd0 + 64 * hf) = pack8(o); } }
.LBB0_570:
	v_mov_b32_e32 v188, s62
	v_and_b32_e32 v188, 0x380, v188
	v_or_b32_e32 v188, v188, v134
	v_lshlrev_b32_e32 v188, 2, v188
	global_load_dword v188, v188, s[60:61]
	global_load_dwordx4 v[4:7], v[132:133], off
	global_load_dwordx4 v[8:11], v[132:133], off offset:16
	ds_read2_b32 v[0:1], v166 offset1:32
	ds_read_b32 v3, v166 offset:256
	ds_read_b32 v21, v172
	v_lshlrev_b32_e32 v22, 16, v76
	v_lshlrev_b32_e32 v24, 16, v78
	v_lshlrev_b32_e32 v26, 16, v77
	v_lshlrev_b32_e32 v28, 16, v79
	s_lshl_b32 s44, s70, 3
	s_lshl_b32 s45, s70, 6
	v_and_b32_e32 v23, 0xffff0000, v76
	v_and_b32_e32 v25, 0xffff0000, v78
	v_and_b32_e32 v27, 0xffff0000, v77
	v_and_b32_e32 v29, 0xffff0000, v79
	v_mul_f32_e32 v2, 0xbfb8aa3b, v22
	v_mul_f32_e32 v30, 0xbfb8aa3b, v24
	v_mul_f32_e32 v76, 0xbfb8aa3b, v26
	v_mul_f32_e32 v78, 0xbfb8aa3b, v28
	s_and_b32 s44, s44, 0xffffe000
	s_and_b32 s45, s45, 0x1fc0
	v_mul_f32_e32 v20, 0xbfb8aa3b, v23
	v_mul_f32_e32 v31, 0xbfb8aa3b, v25
	v_mul_f32_e32 v77, 0xbfb8aa3b, v27
	v_mul_f32_e32 v79, 0xbfb8aa3b, v29
	v_exp_f32_e32 v88, v2
	v_exp_f32_e32 v90, v30
	v_exp_f32_e32 v76, v76
	v_exp_f32_e32 v78, v78
	s_or_b32 s44, s44, s45
	v_exp_f32_e32 v89, v20
	v_exp_f32_e32 v91, v31
	v_exp_f32_e32 v77, v77
	v_exp_f32_e32 v79, v79
	v_add_u32_e32 v30, s44, v120
	s_waitcnt lgkmcnt(2)
	v_mov_b32_e32 v2, v0
	v_mov_b32_e32 v20, v1
	v_ashrrev_i32_e32 v31, 31, v30
	s_waitcnt lgkmcnt(0)
	v_pk_add_f32 v[2:3], v[2:3], v[20:21]
	v_lshlrev_b64 v[0:1], 12, v[30:31]
	v_add_f32_e32 v20, 1.0, v88
	v_add_f32_e32 v30, 1.0, v90
	v_add_f32_e32 v76, 1.0, v76
	v_add_f32_e32 v78, 1.0, v78
	v_add_f32_e32 v88, v2, v3
	v_add_f32_e32 v21, 1.0, v89
	v_add_f32_e32 v31, 1.0, v91
	v_add_f32_e32 v77, 1.0, v77
	v_add_f32_e32 v79, 1.0, v79
	v_rcp_f32_e32 v2, v20
	v_rcp_f32_e32 v20, v30
	v_rcp_f32_e32 v30, v76
	v_rcp_f32_e32 v76, v78
	v_fmamk_f32 v78, v88, 0x3c000000, v179
	s_mov_b32 s44, 0x800000
	v_rcp_f32_e32 v3, v21
	v_rcp_f32_e32 v21, v31
	v_rcp_f32_e32 v31, v77
	v_rcp_f32_e32 v77, v79
	v_mul_f32_e32 v79, 0x4b800000, v78
	v_cmp_gt_f32_e32 vcc, s44, v78
	ds_read_b128 v[12:15], v180
	ds_read_b128 v[16:19], v180 offset:16
	v_cndmask_b32_e32 v78, v78, v79, vcc
	v_rsq_f32_e32 v78, v78
	v_pk_mul_f32 v[22:23], v[2:3], v[22:23]
	s_lshl_b32 s66, s66, 1
	v_lshl_add_u64 v[0:1], s[46:47], 0, v[0:1]
	v_mul_f32_e32 v2, 0x45800000, v78
	v_cndmask_b32_e32 v2, v78, v2, vcc
	s_waitcnt lgkmcnt(1)
	v_pk_mul_f32 v[12:13], v[12:13], v[2:3] op_sel_hi:[1,0]
	s_waitcnt lgkmcnt(0)
	v_pk_mul_f32 v[16:17], v[16:17], v[2:3] op_sel_hi:[1,0]
	v_pk_mul_f32 v[14:15], v[14:15], v[2:3] op_sel_hi:[1,0]
	v_lshl_add_u64 v[0:1], v[0:1], 0, s[66:67]
	v_pk_mul_f32 v[20:21], v[20:21], v[24:25]
	v_pk_mul_f32 v[24:25], v[30:31], v[26:27]
	v_lshl_add_u64 v[0:1], v[0:1], 0, v[124:125]
	s_mov_b32 s44, 0x37500000
	v_lshlrev_b32_e32 v26, 16, v75
	v_and_b32_e32 v27, 0xffff0000, v75
	v_mul_f32_e32 v89, 0xbfb8aa3b, v26
	v_mul_f32_e32 v90, 0xbfb8aa3b, v27
	v_exp_f32_e32 v89, v89
	s_waitcnt vmcnt(1)
	v_pk_mul_f32 v[4:5], v[4:5], v[12:13]
	s_waitcnt vmcnt(0)
	v_pk_mul_f32 v[8:9], v[8:9], v[16:17]
	v_pk_mul_f32 v[6:7], v[6:7], v[14:15]
	v_pk_mul_f32 v[12:13], v[18:19], v[2:3] op_sel_hi:[1,0]
	v_pk_mul_f32 v[4:5], v[22:23], v[4:5]
	v_pk_mul_f32 v[8:9], v[20:21], v[8:9]
	v_pk_mul_f32 v[6:7], v[24:25], v[6:7]
	v_pk_mul_f32 v[10:11], v[10:11], v[12:13]
	v_pk_mul_f32 v[12:13], v[76:77], v[28:29]
	v_cvt_pk_bf16_f32 v4, v4, v5
	v_pk_mul_f32 v[10:11], v[12:13], v[10:11]
	v_cvt_pk_bf16_f32 v5, v6, v7
	v_cvt_pk_bf16_f32 v6, v8, v9
	v_add_co_u32_e32 v8, vcc, s44, v0
	v_cvt_pk_bf16_f32 v7, v10, v11
	s_nop 0
	v_addc_co_u32_e32 v9, vcc, 0, v1, vcc
	global_store_dwordx4 v[8:9], v[4:7], off offset:2048
	global_load_dwordx4 v[4:7], v[132:133], off offset:256
	s_nop 0
	global_load_dwordx4 v[8:11], v[132:133], off offset:272
	v_lshlrev_b32_e32 v20, 16, v72
	v_and_b32_e32 v21, 0xffff0000, v72
	v_lshlrev_b32_e32 v22, 16, v74
	v_and_b32_e32 v23, 0xffff0000, v74
	v_lshlrev_b32_e32 v24, 16, v73
	v_and_b32_e32 v25, 0xffff0000, v73
	v_mul_f32_e32 v3, 0xbfb8aa3b, v20
	v_mul_f32_e32 v28, 0xbfb8aa3b, v21
	v_mul_f32_e32 v29, 0xbfb8aa3b, v22
	v_mul_f32_e32 v30, 0xbfb8aa3b, v23
	v_mul_f32_e32 v31, 0xbfb8aa3b, v24
	v_mul_f32_e32 v88, 0xbfb8aa3b, v25
	v_exp_f32_e32 v3, v3
	v_exp_f32_e32 v28, v28
	v_exp_f32_e32 v29, v29
	v_exp_f32_e32 v30, v30
	v_exp_f32_e32 v31, v31
	v_exp_f32_e32 v88, v88
	v_exp_f32_e32 v90, v90
	ds_read_b128 v[12:15], v180 offset:256
	ds_read_b128 v[16:19], v180 offset:272
	v_add_f32_e32 v3, 1.0, v3
	v_add_f32_e32 v91, 1.0, v28
	v_add_f32_e32 v92, 1.0, v29
	v_add_f32_e32 v93, 1.0, v30
	v_add_f32_e32 v94, 1.0, v31
	v_add_f32_e32 v95, 1.0, v88
	v_add_f32_e32 v96, 1.0, v89
	v_add_f32_e32 v97, 1.0, v90
	v_rcp_f32_e32 v28, v3
	v_rcp_f32_e32 v29, v91
	v_rcp_f32_e32 v30, v92
	v_rcp_f32_e32 v31, v93
	v_rcp_f32_e32 v88, v94
	v_rcp_f32_e32 v89, v95
	v_rcp_f32_e32 v90, v96
	v_rcp_f32_e32 v91, v97
	s_mov_b64 s[44:45], 0x37500800
	s_waitcnt lgkmcnt(1)
	v_pk_mul_f32 v[12:13], v[2:3], v[12:13] op_sel_hi:[0,1]
	s_waitcnt lgkmcnt(0)
	v_pk_mul_f32 v[16:17], v[2:3], v[16:17] op_sel_hi:[0,1]
	v_pk_mul_f32 v[14:15], v[2:3], v[14:15] op_sel_hi:[0,1]
	v_pk_mul_f32 v[2:3], v[2:3], v[18:19] op_sel_hi:[0,1]
	v_lshl_add_u64 v[92:93], v[0:1], 0, s[44:45]
	v_pk_mul_f32 v[0:1], v[28:29], v[20:21]
	v_pk_mul_f32 v[20:21], v[30:31], v[22:23]
	v_pk_mul_f32 v[22:23], v[88:89], v[24:25]
	v_pk_mul_f32 v[24:25], v[90:91], v[26:27]
	v_mov_b64_e32 v[76:77], v[84:85]
	v_mov_b64_e32 v[72:73], v[80:81]
	v_mov_b64_e32 v[78:79], v[86:87]
	v_mov_b64_e32 v[74:75], v[82:83]
	s_andn2_b64 vcc, exec, s[78:79]
	s_mov_b32 s70, s62
	s_waitcnt vmcnt(1)
	v_pk_mul_f32 v[4:5], v[12:13], v[4:5]
	s_waitcnt vmcnt(0)
	v_pk_mul_f32 v[8:9], v[16:17], v[8:9]
	v_pk_mul_f32 v[6:7], v[14:15], v[6:7]
	v_pk_mul_f32 v[2:3], v[2:3], v[10:11]
	v_pk_mul_f32 v[0:1], v[0:1], v[4:5]
	v_pk_mul_f32 v[4:5], v[20:21], v[8:9]
	v_pk_mul_f32 v[6:7], v[22:23], v[6:7]
	v_pk_mul_f32 v[8:9], v[24:25], v[2:3]
	v_cvt_pk_bf16_f32 v0, v0, v1
	v_cvt_pk_bf16_f32 v1, v6, v7
	v_cvt_pk_bf16_f32 v2, v4, v5
	v_cvt_pk_bf16_f32 v3, v8, v9
	global_store_dwordx4 v[92:93], v[0:3], off offset:128
	s_cbranch_vccz .LBB0_583

; __device__ __forceinline__ float bf2f(bf16 b) { return __uint_as_float(((unsigned)b) << 16); }
; __device__ __forceinline__ float sigmoidf_(float x) { return __builtin_amdgcn_rcpf(1.0f + __builtin_amdgcn_exp2f(-1.4426950408889634f * x)); }
; __device__ __forceinline__ void ph_hgO(const Ctx& c) {
;     ...
;         const float lbv = lb[h * 128 + d];
;         float cs[16], kk[16]; float run = 0.f;
; #pragma unroll
;         for (int i = 0; i < 16; ++i) { const float f = lbv + (1.0f - lbv) * sigmoidf_(bf2f(fl[i])); kk[i] = 1.0f - f; run += __builtin_amdgcn_logf(f); cs[i] = run; }
;         SS[seg * 128 + d] = run;
;         __syncthreads();
;         { const float s0 = SS[d], s1 = SS[128 + d], s2 = SS[256 + d];
;           const float prefix = (seg > 0 ? s0 : 0.f) + (seg > 1 ? s1 : 0.f) + (seg > 2 ? s2 : 0.f), ref = s0 + s1;
.LBB0_573:
	s_and_b32 s66, s70, 0x380
	v_lshlrev_b32_e32 v0, 16, v136
	v_lshlrev_b32_e32 v1, 16, v137
	v_mul_f32_e32 v0, 0xbfb8aa3b, v0
	v_mul_f32_e32 v1, 0xbfb8aa3b, v1
	v_exp_f32_e32 v0, v0
	v_exp_f32_e32 v1, v1
	v_lshlrev_b32_e32 v3, 16, v138
	v_lshlrev_b32_e32 v4, 16, v139
	v_mul_f32_e32 v3, 0xbfb8aa3b, v3
	v_lshlrev_b32_e32 v5, 16, v140
	v_mul_f32_e32 v4, 0xbfb8aa3b, v4
	v_exp_f32_e32 v3, v3
	v_add_f32_e32 v0, 1.0, v0
	v_lshlrev_b32_e32 v6, 16, v141
	v_mul_f32_e32 v5, 0xbfb8aa3b, v5
	v_exp_f32_e32 v4, v4
	v_add_f32_e32 v1, 1.0, v1
	v_rcp_f32_e32 v0, v0
	v_lshlrev_b32_e32 v7, 16, v142
	v_mul_f32_e32 v6, 0xbfb8aa3b, v6
	v_exp_f32_e32 v5, v5
	v_rcp_f32_e32 v1, v1
	v_lshlrev_b32_e32 v8, 16, v143
	v_mul_f32_e32 v7, 0xbfb8aa3b, v7
	v_exp_f32_e32 v6, v6
	v_lshlrev_b32_e32 v9, 16, v152
	v_mul_f32_e32 v8, 0xbfb8aa3b, v8
	v_exp_f32_e32 v7, v7
	v_add_f32_e32 v3, 1.0, v3
	v_lshlrev_b32_e32 v10, 16, v153
	v_mul_f32_e32 v9, 0xbfb8aa3b, v9
	v_exp_f32_e32 v8, v8
	v_add_f32_e32 v4, 1.0, v4
	v_rcp_f32_e32 v3, v3
	v_lshlrev_b32_e32 v11, 16, v154
	v_mul_f32_e32 v10, 0xbfb8aa3b, v10
	v_exp_f32_e32 v9, v9
	v_add_f32_e32 v5, 1.0, v5
	v_rcp_f32_e32 v4, v4
	v_lshlrev_b32_e32 v12, 16, v155
	v_mul_f32_e32 v11, 0xbfb8aa3b, v11
	v_exp_f32_e32 v10, v10
	v_add_f32_e32 v6, 1.0, v6
	v_rcp_f32_e32 v5, v5
	v_lshlrev_b32_e32 v13, 16, v156
	v_mul_f32_e32 v12, 0xbfb8aa3b, v12
	v_exp_f32_e32 v11, v11
	v_add_f32_e32 v7, 1.0, v7
	v_rcp_f32_e32 v6, v6
	v_mul_f32_e32 v13, 0xbfb8aa3b, v13
	v_exp_f32_e32 v12, v12
	v_add_f32_e32 v8, 1.0, v8
	v_rcp_f32_e32 v7, v7
	v_add_f32_e32 v9, 1.0, v9
	v_rcp_f32_e32 v8, v8
	v_add_f32_e32 v10, 1.0, v10
	v_rcp_f32_e32 v9, v9
	v_lshlrev_b32_e32 v28, 16, v160
	v_lshlrev_b32_e32 v29, 16, v161
	v_add_f32_e32 v11, 1.0, v11
	v_rcp_f32_e32 v10, v10
	v_mul_f32_e32 v28, 0xbfb8aa3b, v28
	v_mul_f32_e32 v29, 0xbfb8aa3b, v29
	v_add_f32_e32 v12, 1.0, v12
	v_rcp_f32_e32 v11, v11
	v_exp_f32_e32 v28, v28
	v_exp_f32_e32 v29, v29
	v_rcp_f32_e32 v12, v12
	s_andn2_b64 vcc, exec, s[84:85]
	v_add_f32_e32 v28, 1.0, v28
	v_add_f32_e32 v29, 1.0, v29
	v_rcp_f32_e32 v28, v28
	v_rcp_f32_e32 v29, v29
	v_mov_b32_e32 v2, v188
	v_sub_f32_e32 v14, 1.0, v2
	v_fma_f32 v15, v0, v14, v2
	v_fma_f32 v16, v1, v14, v2
	v_log_f32_e32 v0, v15
	v_log_f32_e32 v1, v16
	v_fma_f32 v3, v3, v14, v2
	v_fma_f32 v4, v4, v14, v2
	v_log_f32_e32 v17, v3
	v_add_f32_e32 v26, 0, v0
	v_exp_f32_e32 v0, v13
	v_fma_f32 v5, v5, v14, v2
	v_log_f32_e32 v18, v4
	v_add_f32_e32 v27, v1, v26
	v_lshlrev_b32_e32 v1, 16, v158
	v_fma_f32 v6, v6, v14, v2
	v_log_f32_e32 v19, v5
	v_mul_f32_e32 v1, 0xbfb8aa3b, v1
	v_fma_f32 v7, v7, v14, v2
	v_log_f32_e32 v20, v6
	v_exp_f32_e32 v1, v1
	v_fma_f32 v8, v8, v14, v2
	v_log_f32_e32 v21, v7
	v_add_f32_e32 v17, v17, v27
	v_add_f32_e32 v0, 1.0, v0
	v_fma_f32 v9, v9, v14, v2
	v_log_f32_e32 v22, v8
	v_add_f32_e32 v18, v18, v17
	v_rcp_f32_e32 v0, v0
	v_fma_f32 v10, v10, v14, v2
	v_log_f32_e32 v23, v9
	v_add_f32_e32 v19, v19, v18
	v_fma_f32 v11, v11, v14, v2
	v_log_f32_e32 v24, v10
	v_add_f32_e32 v20, v20, v19
	v_add_f32_e32 v1, 1.0, v1
	v_log_f32_e32 v25, v11
	v_add_f32_e32 v21, v21, v20
	v_fma_f32 v12, v12, v14, v2
	v_rcp_f32_e32 v1, v1
	v_add_f32_e32 v22, v22, v21
	v_log_f32_e32 v13, v12
	v_fma_f32 v30, v0, v14, v2
	v_add_f32_e32 v23, v23, v22
	v_log_f32_e32 v0, v30
	v_add_f32_e32 v24, v24, v23
	v_fma_f32 v31, v1, v14, v2
	v_fma_f32 v28, v28, v14, v2
	v_fmac_f32_e32 v2, v29, v14
	v_add_f32_e32 v14, v25, v24
	v_log_f32_e32 v1, v31
	v_add_f32_e32 v13, v13, v14
	v_add_f32_e32 v25, v0, v13
	v_log_f32_e32 v0, v28
	v_add_f32_e32 v29, v1, v25
	v_sub_f32_e32 v15, 1.0, v15
	v_sub_f32_e32 v3, 1.0, v3
	v_add_f32_e32 v88, v0, v29
	v_log_f32_e32 v0, v2
	v_sub_f32_e32 v4, 1.0, v4
	v_sub_f32_e32 v5, 1.0, v5
	v_sub_f32_e32 v6, 1.0, v6
	v_add_f32_e32 v89, v0, v88
	ds_write_b32 v157, v89
	s_waitcnt lgkmcnt(0)
	s_barrier
	ds_read2st64_b32 v[0:1], v159 offset1:2
	v_sub_f32_e32 v7, 1.0, v7
	v_sub_f32_e32 v8, 1.0, v8
	v_sub_f32_e32 v9, 1.0, v9
	v_sub_f32_e32 v10, 1.0, v10
	s_waitcnt lgkmcnt(0)
	v_cndmask_b32_e64 v90, 0, v0, s[0:1]
	v_cndmask_b32_e64 v91, 0, v1, s[4:5]
	v_add_f32_e32 v90, v90, v91
	ds_read_b32 v91, v159 offset:1024
	v_add_f32_e32 v0, v0, v1
	v_sub_f32_e32 v11, 1.0, v11
	v_sub_f32_e32 v12, 1.0, v12
	v_sub_f32_e32 v2, 1.0, v2
	s_waitcnt lgkmcnt(0)
; __device__ __forceinline__ float bf2f(bf16 b) { return __uint_as_float(((unsigned)b) << 16); }
; __device__ __forceinline__ void ph_hgO(const Ctx& c) {
;     ...
;           for (int i = 0; i < 16; ++i) { const float bb = prefix + cs[i], q = bf2f(qq[i]); const int t = 16 * seg + i;
;               QB[t * 136 + d] = f2bf(q * __builtin_amdgcn_exp2f(bb)); QS[t * 136 + d] = f2bf(q * __builtin_amdgcn_exp2f(bb - ref)); KS[t * 136 + d] = f2bf(kk[i] * __builtin_amdgcn_exp2f(ref - bb)); }
	v_cndmask_b32_e64 v91, 0, v91, s[6:7]
	v_add_f32_e32 v90, v90, v91
	v_add_f32_e32 v1, v26, v90
	v_exp_f32_e32 v26, v1
	v_lshlrev_b32_e32 v91, 16, v144
	v_mul_f32_e32 v26, v26, v91
	v_cvt_pk_bf16_f32 v26, v26, s0
	ds_write_b16 v173, v26
	v_sub_f32_e32 v26, v1, v0
	v_sub_f32_e32 v1, v0, v1
	v_exp_f32_e32 v1, v1
	v_exp_f32_e32 v26, v26
	v_mul_f32_e32 v1, v15, v1
	v_cvt_pk_bf16_f32 v1, v1, s0
	ds_write_b16 v173, v1 offset:34816
	v_add_f32_e32 v1, v27, v90
	v_exp_f32_e32 v15, v1
	v_mul_f32_e32 v26, v26, v91
	v_cvt_pk_bf16_f32 v26, v26, s0
	ds_write_b16 v173, v26 offset:17408
	v_lshlrev_b32_e32 v26, 16, v145
	v_mul_f32_e32 v15, v15, v26
	v_cvt_pk_bf16_f32 v15, v15, s0
	ds_write_b16 v173, v15 offset:272
	v_sub_f32_e32 v15, v1, v0
	v_exp_f32_e32 v15, v15
	v_sub_f32_e32 v1, v0, v1
	v_exp_f32_e32 v1, v1
	v_mul_f32_e32 v15, v15, v26
	v_cvt_pk_bf16_f32 v15, v15, s0
	ds_write_b16 v173, v15 offset:17680
	v_sub_f32_e32 v15, 1.0, v16
	v_mul_f32_e32 v1, v15, v1
	v_cvt_pk_bf16_f32 v1, v1, s0
	ds_write_b16 v173, v1 offset:35088
	v_add_f32_e32 v1, v17, v90
	v_exp_f32_e32 v15, v1
	v_lshlrev_b32_e32 v16, 16, v146
	v_sub_f32_e32 v17, 1.0, v28
	v_mul_f32_e32 v15, v15, v16
	v_cvt_pk_bf16_f32 v15, v15, s0
	ds_write_b16 v173, v15 offset:544
	v_sub_f32_e32 v15, v1, v0
	v_sub_f32_e32 v1, v0, v1
	v_exp_f32_e32 v1, v1
	v_exp_f32_e32 v15, v15
	v_mul_f32_e32 v1, v3, v1
	v_add_f32_e32 v3, v18, v90
	v_exp_f32_e32 v18, v3
	v_cvt_pk_bf16_f32 v1, v1, s0
	ds_write_b16 v173, v1 offset:35360
	v_lshlrev_b32_e32 v1, 16, v147
	v_mul_f32_e32 v18, v18, v1
	v_cvt_pk_bf16_f32 v18, v18, s0
	ds_write_b16 v173, v18 offset:816
	v_sub_f32_e32 v18, v3, v0
	v_exp_f32_e32 v18, v18
	v_sub_f32_e32 v3, v0, v3
	v_exp_f32_e32 v3, v3
	v_mul_f32_e32 v15, v15, v16
	v_mul_f32_e32 v1, v18, v1
	v_cvt_pk_bf16_f32 v1, v1, s0
	ds_write_b16 v173, v1 offset:18224
	v_mul_f32_e32 v1, v4, v3
	v_add_f32_e32 v3, v90, v19
	v_sub_f32_e32 v18, v3, v0
	v_exp_f32_e32 v4, v3
	v_exp_f32_e32 v18, v18
	v_sub_f32_e32 v3, v0, v3
	v_cvt_pk_bf16_f32 v1, v1, s0
	v_exp_f32_e32 v3, v3
	ds_write_b16 v173, v1 offset:35632
	v_lshlrev_b32_e32 v1, 16, v148
	v_mul_f32_e32 v4, v4, v1
	v_mul_f32_e32 v1, v18, v1
	v_cvt_pk_bf16_f32 v1, v1, s0
	ds_write_b16 v173, v1 offset:18496
	v_mul_f32_e32 v1, v5, v3
	v_add_f32_e32 v3, v90, v20
	v_cvt_pk_bf16_f32 v4, v4, s0
	v_sub_f32_e32 v5, v3, v0
	ds_write_b16 v173, v4 offset:1088
	v_exp_f32_e32 v4, v3
	v_exp_f32_e32 v5, v5
	v_sub_f32_e32 v3, v0, v3
	v_cvt_pk_bf16_f32 v1, v1, s0
	v_exp_f32_e32 v3, v3
	ds_write_b16 v173, v1 offset:35904
	v_lshlrev_b32_e32 v1, 16, v149
	v_mul_f32_e32 v4, v4, v1
	v_mul_f32_e32 v1, v5, v1
	v_cvt_pk_bf16_f32 v1, v1, s0
	ds_write_b16 v173, v1 offset:18768
	v_mul_f32_e32 v1, v6, v3
	v_add_f32_e32 v3, v90, v21
	v_cvt_pk_bf16_f32 v4, v4, s0
	v_sub_f32_e32 v5, v3, v0
	ds_write_b16 v173, v4 offset:1360
	v_exp_f32_e32 v4, v3
	v_exp_f32_e32 v5, v5
	v_sub_f32_e32 v3, v0, v3
	v_cvt_pk_bf16_f32 v1, v1, s0
	v_exp_f32_e32 v3, v3
	ds_write_b16 v173, v1 offset:36176
	v_lshlrev_b32_e32 v1, 16, v150
	v_mul_f32_e32 v4, v4, v1
	v_mul_f32_e32 v1, v5, v1
	v_cvt_pk_bf16_f32 v1, v1, s0
	ds_write_b16 v173, v1 offset:19040
	v_mul_f32_e32 v1, v7, v3
	v_add_f32_e32 v3, v90, v22
	v_cvt_pk_bf16_f32 v4, v4, s0
	v_sub_f32_e32 v5, v3, v0
	ds_write_b16 v173, v4 offset:1632
	v_exp_f32_e32 v4, v3
	v_exp_f32_e32 v5, v5
	v_sub_f32_e32 v3, v0, v3
	v_cvt_pk_bf16_f32 v1, v1, s0
	v_exp_f32_e32 v3, v3
	ds_write_b16 v173, v1 offset:36448
	v_lshlrev_b32_e32 v1, 16, v151
	v_mul_f32_e32 v4, v4, v1
	v_mul_f32_e32 v1, v5, v1
	v_cvt_pk_bf16_f32 v1, v1, s0
	ds_write_b16 v173, v1 offset:19312
	v_mul_f32_e32 v1, v8, v3
	v_add_f32_e32 v3, v90, v23
	v_cvt_pk_bf16_f32 v4, v4, s0
	v_sub_f32_e32 v5, v3, v0
	ds_write_b16 v173, v4 offset:1904
	v_exp_f32_e32 v4, v3
	v_exp_f32_e32 v5, v5
	v_sub_f32_e32 v3, v0, v3
	v_cvt_pk_bf16_f32 v1, v1, s0
	v_exp_f32_e32 v3, v3
	ds_write_b16 v173, v1 offset:36720
	v_lshlrev_b32_e32 v1, 16, v162
	v_mul_f32_e32 v4, v4, v1
	v_mul_f32_e32 v1, v5, v1
	v_cvt_pk_bf16_f32 v1, v1, s0
	ds_write_b16 v173, v1 offset:19584
	v_mul_f32_e32 v1, v9, v3
	v_add_f32_e32 v3, v90, v24
	v_cvt_pk_bf16_f32 v4, v4, s0
	v_sub_f32_e32 v5, v3, v0
	ds_write_b16 v173, v4 offset:2176
	v_exp_f32_e32 v4, v3
	v_exp_f32_e32 v5, v5
	v_sub_f32_e32 v3, v0, v3
	v_cvt_pk_bf16_f32 v1, v1, s0
	v_exp_f32_e32 v3, v3
	ds_write_b16 v173, v1 offset:36992
	v_lshlrev_b32_e32 v1, 16, v163
	v_mul_f32_e32 v4, v4, v1
	v_mul_f32_e32 v1, v5, v1
	v_cvt_pk_bf16_f32 v1, v1, s0
	ds_write_b16 v173, v1 offset:19856
	v_mul_f32_e32 v1, v10, v3
	v_add_f32_e32 v3, v90, v14
	v_cvt_pk_bf16_f32 v4, v4, s0
	v_sub_f32_e32 v5, v3, v0
	ds_write_b16 v173, v4 offset:2448
	v_exp_f32_e32 v4, v3
	v_exp_f32_e32 v5, v5
	v_sub_f32_e32 v3, v0, v3
; #define LAS __attribute__((address_space(3)))
; __device__ __forceinline__ float bf2f(bf16 b) { return __uint_as_float(((unsigned)b) << 16); }
; #define HGO_LOAD_S(U) do { const bf16* _sp = SIN + (size_t)(U) * 16384 + (32 * vdt + r) * 128 + 8 * hh; _Pragma("unroll") for (int k8 = 0; k8 < 8; ++k8) sfr[k8] = *(const bf16x8*)(_sp + 16 * k8); } while (0)
; __device__ __forceinline__ void ph_hgO(const Ctx& c) {
;     ...
;           for (int i = 0; i < 16; ++i) { const float bb = prefix + cs[i], q = bf2f(qq[i]); const int t = 16 * seg + i;
;               QB[t * 136 + d] = f2bf(q * __builtin_amdgcn_exp2f(bb)); QS[t * 136 + d] = f2bf(q * __builtin_amdgcn_exp2f(bb - ref)); KS[t * 136 + d] = f2bf(kk[i] * __builtin_amdgcn_exp2f(ref - bb)); }
;           *(LAS u32x4*)(VT + d * 72 + 16 * seg) = pk8us(vv[0], vv[1], vv[2], vv[3], vv[8], vv[9], vv[10], vv[11]);
;           *(LAS u32x4*)(VT + d * 72 + 16 * seg + 8) = pk8us(vv[4], vv[5], vv[6], vv[7], vv[12], vv[13], vv[14], vv[15]); }
;         __syncthreads();
;         f32x16 acc;
; #pragma unroll
;         for (int i = 0; i < 16; ++i) acc[i] = 0.f;
; #pragma unroll
;         for (int k8 = 0; k8 < 8; ++k8) { const bf16x8 bq = *(const LAS bf16x8*)(QB + (32 * tt + r) * 136 + 16 * k8 + 8 * hh); acc = __builtin_amdgcn_mfma_f32_32x32x16_bf16(sfr[k8], bq, acc, 0, 0, 0); }
;         if (u + c.G < 2048) HGO_LOAD_S(u + c.G);
	v_cvt_pk_bf16_f32 v1, v1, s0
	v_exp_f32_e32 v3, v3
	ds_write_b16 v173, v1 offset:37264
	v_lshlrev_b32_e32 v1, 16, v164
	v_mul_f32_e32 v4, v4, v1
	v_mul_f32_e32 v1, v5, v1
	v_cvt_pk_bf16_f32 v1, v1, s0
	ds_write_b16 v173, v1 offset:20128
	v_mul_f32_e32 v1, v11, v3
	v_add_f32_e32 v3, v90, v13
	v_cvt_pk_bf16_f32 v4, v4, s0
	v_sub_f32_e32 v5, v3, v0
	ds_write_b16 v173, v4 offset:2720
	v_exp_f32_e32 v4, v3
	v_exp_f32_e32 v5, v5
	v_sub_f32_e32 v3, v0, v3
	v_cvt_pk_bf16_f32 v1, v1, s0
	v_exp_f32_e32 v3, v3
	ds_write_b16 v173, v1 offset:37536
	v_lshlrev_b32_e32 v1, 16, v165
	v_mul_f32_e32 v4, v4, v1
	v_mul_f32_e32 v1, v5, v1
	v_cvt_pk_bf16_f32 v1, v1, s0
	ds_write_b16 v173, v1 offset:20400
	v_mul_f32_e32 v1, v12, v3
	v_add_f32_e32 v3, v90, v25
	v_cvt_pk_bf16_f32 v4, v4, s0
	v_sub_f32_e32 v5, v3, v0
	ds_write_b16 v173, v4 offset:2992
	v_exp_f32_e32 v4, v3
	v_exp_f32_e32 v5, v5
	v_sub_f32_e32 v3, v0, v3
	v_cvt_pk_bf16_f32 v1, v1, s0
	v_exp_f32_e32 v3, v3
	ds_write_b16 v173, v1 offset:37808
	v_lshlrev_b32_e32 v1, 16, v167
	v_cvt_pk_bf16_f32 v15, v15, s0
	v_mul_f32_e32 v4, v4, v1
	v_mul_f32_e32 v1, v5, v1
	ds_write_b16 v173, v15 offset:17952
	v_sub_f32_e32 v15, 1.0, v30
	v_cvt_pk_bf16_f32 v1, v1, s0
	ds_write_b16 v173, v1 offset:20672
	v_mul_f32_e32 v1, v15, v3
	v_add_f32_e32 v3, v90, v29
	v_cvt_pk_bf16_f32 v4, v4, s0
	v_sub_f32_e32 v5, v3, v0
	ds_write_b16 v173, v4 offset:3264
	v_exp_f32_e32 v4, v3
	v_exp_f32_e32 v5, v5
	v_sub_f32_e32 v3, v0, v3
	v_cvt_pk_bf16_f32 v1, v1, s0
	v_exp_f32_e32 v3, v3
	ds_write_b16 v173, v1 offset:38080
	v_lshlrev_b32_e32 v1, 16, v168
	v_mul_f32_e32 v4, v4, v1
	v_mul_f32_e32 v1, v5, v1
	v_sub_f32_e32 v16, 1.0, v31
	v_cvt_pk_bf16_f32 v1, v1, s0
	ds_write_b16 v173, v1 offset:20944
	v_mul_f32_e32 v1, v16, v3
	v_add_f32_e32 v3, v90, v88
	v_cvt_pk_bf16_f32 v4, v4, s0
	v_sub_f32_e32 v5, v3, v0
	ds_write_b16 v173, v4 offset:3536
	v_exp_f32_e32 v4, v3
	v_exp_f32_e32 v5, v5
	v_sub_f32_e32 v3, v0, v3
	v_cvt_pk_bf16_f32 v1, v1, s0
	v_exp_f32_e32 v3, v3
	ds_write_b16 v173, v1 offset:38352
	v_lshlrev_b32_e32 v1, 16, v169
	v_mul_f32_e32 v4, v4, v1
	v_mul_f32_e32 v1, v5, v1
	v_cvt_pk_bf16_f32 v1, v1, s0
	ds_write_b16 v173, v1 offset:21216
	v_mul_f32_e32 v1, v17, v3
	v_add_f32_e32 v3, v90, v89
	v_cvt_pk_bf16_f32 v4, v4, s0
	v_sub_f32_e32 v5, v3, v0
	v_sub_f32_e32 v0, v0, v3
	ds_write_b16 v173, v4 offset:3808
	v_exp_f32_e32 v4, v3
	v_exp_f32_e32 v5, v5
	v_exp_f32_e32 v0, v0
	v_cvt_pk_bf16_f32 v1, v1, s0
	ds_write_b16 v173, v1 offset:38624
	v_lshlrev_b32_e32 v1, 16, v170
	v_mul_f32_e32 v4, v4, v1
	v_mul_f32_e32 v1, v5, v1
	v_mul_f32_e32 v0, v2, v0
	v_cvt_pk_bf16_f32 v1, v1, s0
	v_cvt_pk_bf16_f32 v0, v0, s0
	v_cvt_pk_bf16_f32 v4, v4, s0
	ds_write_b16 v173, v1 offset:21488
	ds_write_b16 v173, v0 offset:38896
	v_mov_b32_e32 v0, v38
	v_mov_b32_e32 v1, v39
	v_mov_b32_e32 v2, v34
	v_mov_b32_e32 v3, v35
	ds_write_b16 v173, v4 offset:4080
	ds_write_b128 v176, v[0:3] offset:52224
	v_mov_b32_e32 v0, v36
	v_mov_b32_e32 v1, v37
	v_mov_b32_e32 v2, v32
	v_mov_b32_e32 v3, v33
	ds_write_b128 v176, v[0:3] offset:52240
	s_waitcnt lgkmcnt(0)
	s_barrier
	ds_read_b128 v[0:3], v181
	ds_read_b128 v[16:19], v181 offset:32
	s_waitcnt lgkmcnt(1)
	v_mfma_f32_32x32x16_bf16 v[0:15], v[40:43], v[0:3], 0
	s_waitcnt lgkmcnt(0)
	v_mfma_f32_32x32x16_bf16 v[0:15], v[44:47], v[16:19], v[0:15]
	ds_read_b128 v[16:19], v181 offset:64
	ds_read_b128 v[20:23], v181 offset:96
	s_waitcnt lgkmcnt(1)
	v_mfma_f32_32x32x16_bf16 v[0:15], v[48:51], v[16:19], v[0:15]
	s_waitcnt lgkmcnt(0)
	v_mfma_f32_32x32x16_bf16 v[0:15], v[52:55], v[20:23], v[0:15]
	ds_read_b128 v[16:19], v181 offset:128
	ds_read_b128 v[20:23], v181 offset:160
	s_waitcnt lgkmcnt(1)
	v_mfma_f32_32x32x16_bf16 v[0:15], v[56:59], v[16:19], v[0:15]
	s_waitcnt lgkmcnt(0)
	v_mfma_f32_32x32x16_bf16 v[0:15], v[60:63], v[20:23], v[0:15]
	ds_read_b128 v[16:19], v181 offset:192
	ds_read_b128 v[20:23], v181 offset:224
	s_waitcnt lgkmcnt(1)
	v_mfma_f32_32x32x16_bf16 v[0:15], v[64:67], v[16:19], v[0:15]
	v_cndmask_b32_e64 v16, 0, 1, s[84:85]
	v_cmp_ne_u32_e64 s[44:45], 1, v16
	s_waitcnt lgkmcnt(0)
	v_mfma_f32_32x32x16_bf16 v[0:15], v[68:71], v[20:23], v[0:15]
	s_cbranch_vccnz .LBB0_575
	s_ashr_i32 s63, s62, 31
	s_lshl_b64 s[84:85], s[62:63], 15
	v_lshl_add_u64 v[16:17], v[130:131], 0, s[84:85]
	global_load_dwordx4 v[40:43], v[16:17], off
	global_load_dwordx4 v[44:47], v[16:17], off offset:32
	global_load_dwordx4 v[48:51], v[16:17], off offset:64
	global_load_dwordx4 v[52:55], v[16:17], off offset:96
	global_load_dwordx4 v[56:59], v[16:17], off offset:128
	global_load_dwordx4 v[60:63], v[16:17], off offset:160
	global_load_dwordx4 v[64:67], v[16:17], off offset:192
	global_load_dwordx4 v[68:71], v[16:17], off offset:224

; #define LAS __attribute__((address_space(3)))
; __device__ __forceinline__ void ph_hgO(const Ctx& c) {
;     ...
;           for (int i4 = 0; i4 < 4; ++i4) *(LAS f32x4*)(OT + (32 * tt + r) * 132 + 32 * vdt + 8 * i4 + 4 * hh) = (f32x4){acc[4 * i4], acc[4 * i4 + 1], acc[4 * i4 + 2], acc[4 * i4 + 3]}; }
;         __syncthreads();
;         if (u + c.G < 2048) HGO_COLS(8);
.LBB0_581:
	s_or_b64 exec, exec, s[84:85]
	s_and_b64 vcc, exec, s[44:45]
	ds_write_b128 v178, v[0:3]
	ds_write_b128 v178, v[4:7] offset:32
	ds_write_b128 v178, v[8:11] offset:64
	ds_write_b128 v178, v[12:15] offset:96
	s_waitcnt lgkmcnt(0)
	s_barrier
	s_cbranch_vccnz .LBB0_570
	s_waitcnt vmcnt(0)
	ds_read_u16 v136, v135
	ds_read_u16 v137, v135 offset:128
	ds_read_u16 v138, v135 offset:256
	ds_read_u16 v139, v135 offset:384
	ds_read_u16 v140, v135 offset:512
	ds_read_u16 v141, v135 offset:640
	ds_read_u16 v142, v135 offset:768
	ds_read_u16 v143, v135 offset:896
	ds_read_u16 v144, v135 offset:2048
	ds_read_u16 v145, v135 offset:2176
	ds_read_u16 v146, v135 offset:2304
	ds_read_u16 v147, v135 offset:2432
	ds_read_u16 v148, v135 offset:2560
	ds_read_u16 v149, v135 offset:2688
	ds_read_u16 v150, v135 offset:2816
	ds_read_u16 v151, v135 offset:2944
	ds_read_u16 v0, v135 offset:4096
	ds_read_u16 v1, v135 offset:4224
	ds_read_u16 v2, v135 offset:4352
	ds_read_u16 v3, v135 offset:4480
	ds_read_u16 v4, v135 offset:4608
	ds_read_u16 v5, v135 offset:4736
	ds_read_u16 v6, v135 offset:4864
	ds_read_u16 v7, v135 offset:4992
	ds_read_u16 v152, v135 offset:1024
	ds_read_u16 v153, v135 offset:1152
	ds_read_u16 v154, v135 offset:1280
	ds_read_u16 v155, v135 offset:1408
	ds_read_u16 v156, v135 offset:1536
	ds_read_u16 v158, v135 offset:1664
	ds_read_u16 v160, v135 offset:1792
	ds_read_u16 v161, v135 offset:1920
	ds_read_u16 v8, v135 offset:5120
	ds_read_u16 v9, v135 offset:5248
	ds_read_u16 v10, v135 offset:5376
	ds_read_u16 v11, v135 offset:5504
	ds_read_u16 v12, v135 offset:5632
	ds_read_u16 v13, v135 offset:5760
	ds_read_u16 v14, v135 offset:5888
	ds_read_u16 v15, v135 offset:6016
	ds_read_u16 v162, v135 offset:3072
	ds_read_u16 v163, v135 offset:3200
	ds_read_u16 v164, v135 offset:3328
	ds_read_u16 v165, v135 offset:3456
	ds_read_u16 v167, v135 offset:3584
	ds_read_u16 v168, v135 offset:3712
	ds_read_u16 v169, v135 offset:3840
	ds_read_u16 v170, v135 offset:3968
	s_waitcnt lgkmcnt(0)
	s_waitcnt lgkmcnt(8)
	v_perm_b32 v33, v15, v14, s3
	v_perm_b32 v32, v13, v12, s3
	v_perm_b32 v35, v11, v10, s3
	v_perm_b32 v34, v9, v8, s3
	v_perm_b32 v37, v7, v6, s3
	v_perm_b32 v36, v5, v4, s3
	v_perm_b32 v39, v3, v2, s3
	v_perm_b32 v38, v1, v0, s3
	s_branch .LBB0_570
